# K-loop critical-segment trimming on top of previous best: scalar prefix of each load segment moved before the post-MFMA barrier, v_mov copies of LDS-DMA offsets removed, redundant lgkmcnt(0) at MFMA s
# baseline (speedup 1.0000x reference)
.LBB0_289:
	s_add_i32 s74, 0, 0x10000
	s_add_i32 s3, 0, 0x14000
	v_add_u32_e32 v140, s74, v225
	v_add_u32_e32 v156, s3, v225
	ds_read_b128 v[128:131], v140
	ds_read_b128 v[132:135], v140 offset:1024
	ds_read_b128 v[136:139], v140 offset:2048
	ds_read_b128 v[140:143], v140 offset:3072
	ds_read_b128 v[144:147], v156
	ds_read_b128 v[148:151], v156 offset:1024
	ds_read_b128 v[152:155], v156 offset:2048
	ds_read_b128 v[156:159], v156 offset:3072
	s_add_i32 vcc_hi, s8, 2
	s_add_u32 s14, s73, 0xffffff80
	s_addc_u32 s15, vcc_lo, -1
	s_add_i32 m0, s91, 0xc000
	s_add_i32 s10, s91, 0xe000
	s_cmp_eq_u32 s88, s8
	s_cselect_b32 s8, s66, s71
	s_cselect_b32 s9, s67, s72
	s_cselect_b32 s19, s65, s68
	s_cselect_b32 s18, s64, s1
	s_cselect_b32 s13, s61, vcc_lo
	s_cselect_b32 s12, s60, s73
	ds_read_b128 v[160:163], v227
	ds_read_b128 v[164:167], v227 offset:1024
	ds_read_b128 v[168:171], v227 offset:2048
	ds_read_b128 v[172:175], v227 offset:3072
	ds_read_b128 v[184:187], v227 offset:4096
	ds_read_b128 v[188:191], v227 offset:5120
	ds_read_b128 v[192:195], v227 offset:6144
	ds_read_b128 v[196:199], v227 offset:7168
	s_nop 0
	global_load_lds_dwordx4 v222, s[14:15]
	s_mov_b32 m0, s10
	s_nop 0
	global_load_lds_dwordx4 v223, s[14:15]
	s_waitcnt vmcnt(8)
	s_waitcnt lgkmcnt(0)
	s_barrier
	s_setprio 1
	v_mfma_f32_16x16x32_bf16 v[124:127], v[128:131], v[160:163], v[124:127]
	v_mfma_f32_16x16x32_bf16 v[120:123], v[136:139], v[160:163], v[120:123]
	v_mfma_f32_16x16x32_bf16 v[108:111], v[128:131], v[168:171], v[108:111]
	v_mfma_f32_16x16x32_bf16 v[104:107], v[136:139], v[168:171], v[104:107]
	v_mfma_f32_16x16x32_bf16 v[92:95], v[128:131], v[184:187], v[92:95]
	v_mfma_f32_16x16x32_bf16 v[88:91], v[136:139], v[184:187], v[88:91]
	v_mfma_f32_16x16x32_bf16 v[76:79], v[128:131], v[192:195], v[76:79]
	v_mfma_f32_16x16x32_bf16 v[72:75], v[136:139], v[192:195], v[72:75]
	v_mfma_f32_16x16x32_bf16 v[124:127], v[132:135], v[164:167], v[124:127]
	v_mfma_f32_16x16x32_bf16 v[120:123], v[140:143], v[164:167], v[120:123]
	v_mfma_f32_16x16x32_bf16 v[108:111], v[132:135], v[172:175], v[108:111]
	v_mfma_f32_16x16x32_bf16 v[104:107], v[140:143], v[172:175], v[104:107]
	v_mfma_f32_16x16x32_bf16 v[92:95], v[132:135], v[188:191], v[92:95]
	v_mfma_f32_16x16x32_bf16 v[88:91], v[140:143], v[188:191], v[88:91]
	v_mfma_f32_16x16x32_bf16 v[76:79], v[132:135], v[196:199], v[76:79]
	v_mfma_f32_16x16x32_bf16 v[72:75], v[140:143], v[196:199], v[72:75]
	s_setprio 0
	s_setprio 1
	v_mfma_f32_16x16x32_bf16 v[116:119], v[144:147], v[160:163], v[116:119]
	v_mfma_f32_16x16x32_bf16 v[112:115], v[152:155], v[160:163], v[112:115]
	v_mfma_f32_16x16x32_bf16 v[100:103], v[144:147], v[168:171], v[100:103]
	v_mfma_f32_16x16x32_bf16 v[96:99], v[152:155], v[168:171], v[96:99]
	v_mfma_f32_16x16x32_bf16 v[84:87], v[144:147], v[184:187], v[84:87]
	v_mfma_f32_16x16x32_bf16 v[80:83], v[152:155], v[184:187], v[80:83]
	v_mfma_f32_16x16x32_bf16 v[68:71], v[144:147], v[192:195], v[68:71]
	v_mfma_f32_16x16x32_bf16 v[64:67], v[152:155], v[192:195], v[64:67]
	v_mfma_f32_16x16x32_bf16 v[116:119], v[148:151], v[164:167], v[116:119]
	v_mfma_f32_16x16x32_bf16 v[112:115], v[156:159], v[164:167], v[112:115]
	v_mfma_f32_16x16x32_bf16 v[100:103], v[148:151], v[172:175], v[100:103]
	v_mfma_f32_16x16x32_bf16 v[96:99], v[156:159], v[172:175], v[96:99]
	v_mfma_f32_16x16x32_bf16 v[84:87], v[148:151], v[188:191], v[84:87]
	v_mfma_f32_16x16x32_bf16 v[80:83], v[156:159], v[188:191], v[80:83]
	v_mfma_f32_16x16x32_bf16 v[68:71], v[148:151], v[196:199], v[68:71]
	v_mfma_f32_16x16x32_bf16 v[64:67], v[156:159], v[196:199], v[64:67]
	s_setprio 0
	s_cselect_b32 s15, s63, s70
	s_cselect_b32 s14, s62, s69
	s_add_i32 s74, s74, s90
	s_barrier
	s_mov_b64 s[10:11], s[18:19]
	s_mov_b32 m0, s74
	ds_read_b128 v[160:163], v227 offset:16384
	ds_read_b128 v[164:167], v227 offset:17408
	ds_read_b128 v[168:171], v227 offset:18432
	ds_read_b128 v[172:175], v227 offset:19456
	ds_read_b128 v[184:187], v227 offset:20480
	ds_read_b128 v[188:191], v227 offset:21504
	ds_read_b128 v[192:195], v227 offset:22528
	ds_read_b128 v[196:199], v227 offset:23552
	s_add_i32 s3, s3, s90
	global_load_lds_dwordx4 v220, s[10:11]
	s_add_i32 m0, s74, 0x2000
	s_nop 0
	global_load_lds_dwordx4 v221, s[10:11]
	s_mov_b64 s[10:11], s[14:15]
	s_mov_b32 m0, s3
	s_nop 0
	global_load_lds_dwordx4 v220, s[10:11]
	s_add_i32 m0, s3, 0x2000
	s_nop 0
	global_load_lds_dwordx4 v221, s[10:11]
	s_mov_b64 s[10:11], s[8:9]
	s_mov_b32 m0, s91
	s_nop 0
	global_load_lds_dwordx4 v222, s[10:11]
	s_mov_b32 m0, s79
	s_nop 0
	global_load_lds_dwordx4 v223, s[10:11]
	s_waitcnt vmcnt(8)
	s_waitcnt lgkmcnt(0)
	s_barrier
	s_setprio 1
	v_mfma_f32_16x16x32_bf16 v[60:63], v[128:131], v[160:163], v[60:63]
	v_mfma_f32_16x16x32_bf16 v[56:59], v[136:139], v[160:163], v[56:59]
	v_mfma_f32_16x16x32_bf16 v[44:47], v[128:131], v[168:171], v[44:47]
	v_mfma_f32_16x16x32_bf16 v[40:43], v[136:139], v[168:171], v[40:43]
	v_mfma_f32_16x16x32_bf16 v[28:31], v[128:131], v[184:187], v[28:31]
	v_mfma_f32_16x16x32_bf16 v[24:27], v[136:139], v[184:187], v[24:27]
	v_mfma_f32_16x16x32_bf16 v[12:15], v[128:131], v[192:195], v[12:15]
	v_mfma_f32_16x16x32_bf16 v[8:11], v[136:139], v[192:195], v[8:11]
	v_mfma_f32_16x16x32_bf16 v[60:63], v[132:135], v[164:167], v[60:63]
	v_mfma_f32_16x16x32_bf16 v[56:59], v[140:143], v[164:167], v[56:59]
	v_mfma_f32_16x16x32_bf16 v[44:47], v[132:135], v[172:175], v[44:47]
	v_mfma_f32_16x16x32_bf16 v[40:43], v[140:143], v[172:175], v[40:43]
	v_mfma_f32_16x16x32_bf16 v[28:31], v[132:135], v[188:191], v[28:31]
	v_mfma_f32_16x16x32_bf16 v[24:27], v[140:143], v[188:191], v[24:27]
	v_mfma_f32_16x16x32_bf16 v[12:15], v[132:135], v[196:199], v[12:15]
	v_mfma_f32_16x16x32_bf16 v[8:11], v[140:143], v[196:199], v[8:11]
	s_setprio 0
	s_setprio 1
	v_mfma_f32_16x16x32_bf16 v[52:55], v[144:147], v[160:163], v[52:55]
	v_mfma_f32_16x16x32_bf16 v[48:51], v[152:155], v[160:163], v[48:51]
	v_mfma_f32_16x16x32_bf16 v[36:39], v[144:147], v[168:171], v[36:39]
	v_mfma_f32_16x16x32_bf16 v[32:35], v[152:155], v[168:171], v[32:35]
	v_mfma_f32_16x16x32_bf16 v[20:23], v[144:147], v[184:187], v[20:23]
	v_mfma_f32_16x16x32_bf16 v[16:19], v[152:155], v[184:187], v[16:19]
	v_mfma_f32_16x16x32_bf16 v[4:7], v[144:147], v[192:195], v[4:7]
	v_mfma_f32_16x16x32_bf16 v[0:3], v[152:155], v[192:195], v[0:3]
	v_mfma_f32_16x16x32_bf16 v[52:55], v[148:151], v[164:167], v[52:55]
	v_mfma_f32_16x16x32_bf16 v[48:51], v[156:159], v[164:167], v[48:51]
	v_mfma_f32_16x16x32_bf16 v[36:39], v[148:151], v[172:175], v[36:39]
	v_mfma_f32_16x16x32_bf16 v[32:35], v[156:159], v[172:175], v[32:35]
	v_mfma_f32_16x16x32_bf16 v[20:23], v[148:151], v[188:191], v[20:23]
	v_mfma_f32_16x16x32_bf16 v[16:19], v[156:159], v[188:191], v[16:19]
	v_mfma_f32_16x16x32_bf16 v[4:7], v[148:151], v[196:199], v[4:7]
	v_mfma_f32_16x16x32_bf16 v[0:3], v[156:159], v[196:199], v[0:3]
	s_setprio 0
	s_add_i32 s3, 0, 0x18000
	s_add_i32 s74, 0, 0x1c000
	s_barrier
	v_add_u32_e32 v140, s3, v225
	v_add_u32_e32 v156, s74, v225
	ds_read_b128 v[128:131], v140
	ds_read_b128 v[132:135], v140 offset:1024
	ds_read_b128 v[136:139], v140 offset:2048
	ds_read_b128 v[140:143], v140 offset:3072
	ds_read_b128 v[144:147], v156
	ds_read_b128 v[148:151], v156 offset:1024
	ds_read_b128 v[152:155], v156 offset:2048
	ds_read_b128 v[156:159], v156 offset:3072
	s_mov_b32 m0, s80
	ds_read_b128 v[160:163], v227 offset:32768
	ds_read_b128 v[164:167], v227 offset:33792
	ds_read_b128 v[168:171], v227 offset:34816
	ds_read_b128 v[172:175], v227 offset:35840
	ds_read_b128 v[184:187], v227 offset:36864
	ds_read_b128 v[188:191], v227 offset:37888
	ds_read_b128 v[192:195], v227 offset:38912
	ds_read_b128 v[196:199], v227 offset:39936
	s_nop 0
	global_load_lds_dwordx4 v222, s[12:13]
	s_mov_b32 m0, s81
	s_nop 0
	global_load_lds_dwordx4 v223, s[12:13]
	s_waitcnt vmcnt(8)
	s_waitcnt lgkmcnt(0)
	s_barrier
	s_setprio 1
	v_mfma_f32_16x16x32_bf16 v[124:127], v[128:131], v[160:163], v[124:127]
	v_mfma_f32_16x16x32_bf16 v[120:123], v[136:139], v[160:163], v[120:123]
	v_mfma_f32_16x16x32_bf16 v[108:111], v[128:131], v[168:171], v[108:111]
	v_mfma_f32_16x16x32_bf16 v[104:107], v[136:139], v[168:171], v[104:107]
	v_mfma_f32_16x16x32_bf16 v[92:95], v[128:131], v[184:187], v[92:95]
	v_mfma_f32_16x16x32_bf16 v[88:91], v[136:139], v[184:187], v[88:91]
	v_mfma_f32_16x16x32_bf16 v[76:79], v[128:131], v[192:195], v[76:79]
	v_mfma_f32_16x16x32_bf16 v[72:75], v[136:139], v[192:195], v[72:75]
	v_mfma_f32_16x16x32_bf16 v[124:127], v[132:135], v[164:167], v[124:127]
	v_mfma_f32_16x16x32_bf16 v[120:123], v[140:143], v[164:167], v[120:123]
	v_mfma_f32_16x16x32_bf16 v[108:111], v[132:135], v[172:175], v[108:111]
	v_mfma_f32_16x16x32_bf16 v[104:107], v[140:143], v[172:175], v[104:107]
	v_mfma_f32_16x16x32_bf16 v[92:95], v[132:135], v[188:191], v[92:95]
	v_mfma_f32_16x16x32_bf16 v[88:91], v[140:143], v[188:191], v[88:91]
	v_mfma_f32_16x16x32_bf16 v[76:79], v[132:135], v[196:199], v[76:79]
	v_mfma_f32_16x16x32_bf16 v[72:75], v[140:143], v[196:199], v[72:75]
	s_setprio 0
	s_setprio 1
	v_mfma_f32_16x16x32_bf16 v[116:119], v[144:147], v[160:163], v[116:119]
	v_mfma_f32_16x16x32_bf16 v[112:115], v[152:155], v[160:163], v[112:115]
	v_mfma_f32_16x16x32_bf16 v[100:103], v[144:147], v[168:171], v[100:103]
	v_mfma_f32_16x16x32_bf16 v[96:99], v[152:155], v[168:171], v[96:99]
	v_mfma_f32_16x16x32_bf16 v[84:87], v[144:147], v[184:187], v[84:87]
	v_mfma_f32_16x16x32_bf16 v[80:83], v[152:155], v[184:187], v[80:83]
	v_mfma_f32_16x16x32_bf16 v[68:71], v[144:147], v[192:195], v[68:71]
	v_mfma_f32_16x16x32_bf16 v[64:67], v[152:155], v[192:195], v[64:67]
	v_mfma_f32_16x16x32_bf16 v[116:119], v[148:151], v[164:167], v[116:119]
	v_mfma_f32_16x16x32_bf16 v[112:115], v[156:159], v[164:167], v[112:115]
	v_mfma_f32_16x16x32_bf16 v[100:103], v[148:151], v[172:175], v[100:103]
	v_mfma_f32_16x16x32_bf16 v[96:99], v[156:159], v[172:175], v[96:99]
	v_mfma_f32_16x16x32_bf16 v[84:87], v[148:151], v[188:191], v[84:87]
	v_mfma_f32_16x16x32_bf16 v[80:83], v[156:159], v[188:191], v[80:83]
	v_mfma_f32_16x16x32_bf16 v[68:71], v[148:151], v[196:199], v[68:71]
	v_mfma_f32_16x16x32_bf16 v[64:67], v[156:159], v[196:199], v[64:67]
	s_setprio 0
	s_add_u32 s10, s18, 0x80
	s_addc_u32 s11, s19, 0
	s_add_i32 s3, s3, s90
	s_barrier
	s_mov_b32 m0, s3
	ds_read_b128 v[160:163], v227 offset:49152
	ds_read_b128 v[164:167], v227 offset:50176
	ds_read_b128 v[168:171], v227 offset:51200
	ds_read_b128 v[172:175], v227 offset:52224
	ds_read_b128 v[184:187], v227 offset:53248
	ds_read_b128 v[188:191], v227 offset:54272
	ds_read_b128 v[192:195], v227 offset:55296
	ds_read_b128 v[196:199], v227 offset:56320
	s_nop 0
	global_load_lds_dwordx4 v220, s[10:11]
	s_add_i32 m0, s3, 0x2000
	s_nop 0
	global_load_lds_dwordx4 v221, s[10:11]
	s_add_u32 s10, s14, 0x80
	s_addc_u32 s11, s15, 0
	s_add_i32 s3, s74, s90
	s_mov_b32 m0, s3
	s_nop 0
	global_load_lds_dwordx4 v220, s[10:11]
	s_add_i32 m0, s3, 0x2000
	s_add_u32 s8, s8, 0x80
	global_load_lds_dwordx4 v221, s[10:11]
	s_addc_u32 s9, s9, 0
	v_mov_b32_e32 v200, v223
	v_mov_b32_e32 v201, v222
	s_mov_b32 m0, s82
	s_nop 0
	global_load_lds_dwordx4 v201, s[8:9]
	s_mov_b32 m0, s34
	s_nop 0
	global_load_lds_dwordx4 v200, s[8:9]
	s_waitcnt vmcnt(8)
	s_waitcnt lgkmcnt(0)
	s_barrier
	s_setprio 1
	v_mfma_f32_16x16x32_bf16 v[60:63], v[128:131], v[160:163], v[60:63]
	v_mfma_f32_16x16x32_bf16 v[56:59], v[136:139], v[160:163], v[56:59]
	v_mfma_f32_16x16x32_bf16 v[44:47], v[128:131], v[168:171], v[44:47]
	v_mfma_f32_16x16x32_bf16 v[40:43], v[136:139], v[168:171], v[40:43]
	v_mfma_f32_16x16x32_bf16 v[28:31], v[128:131], v[184:187], v[28:31]
	v_mfma_f32_16x16x32_bf16 v[24:27], v[136:139], v[184:187], v[24:27]
	v_mfma_f32_16x16x32_bf16 v[12:15], v[128:131], v[192:195], v[12:15]
	v_mfma_f32_16x16x32_bf16 v[8:11], v[136:139], v[192:195], v[8:11]
	v_mfma_f32_16x16x32_bf16 v[60:63], v[132:135], v[164:167], v[60:63]
	v_mfma_f32_16x16x32_bf16 v[56:59], v[140:143], v[164:167], v[56:59]
	v_mfma_f32_16x16x32_bf16 v[44:47], v[132:135], v[172:175], v[44:47]
	v_mfma_f32_16x16x32_bf16 v[40:43], v[140:143], v[172:175], v[40:43]
	v_mfma_f32_16x16x32_bf16 v[28:31], v[132:135], v[188:191], v[28:31]
	v_mfma_f32_16x16x32_bf16 v[24:27], v[140:143], v[188:191], v[24:27]
	v_mfma_f32_16x16x32_bf16 v[12:15], v[132:135], v[196:199], v[12:15]
	v_mfma_f32_16x16x32_bf16 v[8:11], v[140:143], v[196:199], v[8:11]
	s_setprio 0
	s_setprio 1
	v_mfma_f32_16x16x32_bf16 v[52:55], v[144:147], v[160:163], v[52:55]
	v_mfma_f32_16x16x32_bf16 v[48:51], v[152:155], v[160:163], v[48:51]
	v_mfma_f32_16x16x32_bf16 v[36:39], v[144:147], v[168:171], v[36:39]
	v_mfma_f32_16x16x32_bf16 v[32:35], v[152:155], v[168:171], v[32:35]
	v_mfma_f32_16x16x32_bf16 v[20:23], v[144:147], v[184:187], v[20:23]
	v_mfma_f32_16x16x32_bf16 v[16:19], v[152:155], v[184:187], v[16:19]
	v_mfma_f32_16x16x32_bf16 v[4:7], v[144:147], v[192:195], v[4:7]
	v_mfma_f32_16x16x32_bf16 v[0:3], v[152:155], v[192:195], v[0:3]
	v_mfma_f32_16x16x32_bf16 v[52:55], v[148:151], v[164:167], v[52:55]
	v_mfma_f32_16x16x32_bf16 v[48:51], v[156:159], v[164:167], v[48:51]
	v_mfma_f32_16x16x32_bf16 v[36:39], v[148:151], v[172:175], v[36:39]
	v_mfma_f32_16x16x32_bf16 v[32:35], v[156:159], v[172:175], v[32:35]
	v_mfma_f32_16x16x32_bf16 v[20:23], v[148:151], v[188:191], v[20:23]
	v_mfma_f32_16x16x32_bf16 v[16:19], v[156:159], v[188:191], v[16:19]
	v_mfma_f32_16x16x32_bf16 v[4:7], v[148:151], v[196:199], v[4:7]
	v_mfma_f32_16x16x32_bf16 v[0:3], v[156:159], v[196:199], v[0:3]
	s_setprio 0
	s_add_u32 s1, s1, 0x100
	s_addc_u32 s68, s68, 0
	s_add_u32 s69, s69, 0x100
	s_addc_u32 s70, s70, 0
	s_add_u32 s71, s71, 0x100
	s_addc_u32 s72, s72, 0
	s_add_u32 s73, s73, 0x100
	s_addc_u32 vcc_lo, vcc_lo, 0
	s_cmp_ge_i32 vcc_hi, s33
	s_mov_b32 s8, vcc_hi
	s_barrier
	s_cbranch_scc0 .LBB0_289
	s_and_b64 vcc, exec, s[50:51]
	s_cbranch_vccz .LBB0_292

.LBB0_1223:
	ds_read_b128 v[134:137], v141
	ds_read_b128 v[146:149], v141 offset:1024
	ds_read_b128 v[150:153], v141 offset:2048
	ds_read_b128 v[154:157], v141 offset:3072
	ds_read_b128 v[158:161], v142
	ds_read_b128 v[162:165], v142 offset:1024
	ds_read_b128 v[166:169], v142 offset:2048
	ds_read_b128 v[170:173], v142 offset:3072
	s_add_i32 s76, s38, 2
	s_add_u32 s44, s74, 0xffffff80
	s_addc_u32 s45, s75, -1
	s_add_i32 m0, s49, 0xc000
	s_add_i32 s77, s49, 0xe000
	s_cmp_eq_u32 s58, s38
	s_cselect_b32 s38, s34, s72
	s_cselect_b32 s39, s35, s73
	s_cselect_b32 s41, s31, s69
	s_cselect_b32 s40, s30, s68
	s_cselect_b32 s43, s23, s75
	s_cselect_b32 s42, s22, s74
	v_mov_b32_e32 v206, v128
	v_mov_b32_e32 v207, v130
	ds_read_b128 v[174:177], v143
	ds_read_b128 v[178:181], v143 offset:1024
	ds_read_b128 v[182:185], v143 offset:2048
	ds_read_b128 v[186:189], v143 offset:3072
	ds_read_b128 v[190:193], v143 offset:4096
	ds_read_b128 v[194:197], v143 offset:5120
	ds_read_b128 v[198:201], v143 offset:6144
	ds_read_b128 v[202:205], v143 offset:7168
	s_nop 0
	global_load_lds_dwordx4 v206, s[44:45] nt
	s_mov_b32 m0, s77
	s_nop 0
	global_load_lds_dwordx4 v207, s[44:45] nt
	s_waitcnt vmcnt(8)
	s_waitcnt lgkmcnt(0)
	s_barrier
	s_setprio 1
	v_mfma_f32_16x16x32_bf16 v[124:127], v[134:137], v[174:177], v[124:127]
	v_mfma_f32_16x16x32_bf16 v[120:123], v[150:153], v[174:177], v[120:123]
	v_mfma_f32_16x16x32_bf16 v[108:111], v[134:137], v[182:185], v[108:111]
	v_mfma_f32_16x16x32_bf16 v[104:107], v[150:153], v[182:185], v[104:107]
	v_mfma_f32_16x16x32_bf16 v[92:95], v[134:137], v[190:193], v[92:95]
	v_mfma_f32_16x16x32_bf16 v[88:91], v[150:153], v[190:193], v[88:91]
	v_mfma_f32_16x16x32_bf16 v[76:79], v[134:137], v[198:201], v[76:79]
	v_mfma_f32_16x16x32_bf16 v[72:75], v[150:153], v[198:201], v[72:75]
	v_mfma_f32_16x16x32_bf16 v[124:127], v[146:149], v[178:181], v[124:127]
	v_mfma_f32_16x16x32_bf16 v[120:123], v[154:157], v[178:181], v[120:123]
	v_mfma_f32_16x16x32_bf16 v[108:111], v[146:149], v[186:189], v[108:111]
	v_mfma_f32_16x16x32_bf16 v[104:107], v[154:157], v[186:189], v[104:107]
	v_mfma_f32_16x16x32_bf16 v[92:95], v[146:149], v[194:197], v[92:95]
	v_mfma_f32_16x16x32_bf16 v[88:91], v[154:157], v[194:197], v[88:91]
	v_mfma_f32_16x16x32_bf16 v[76:79], v[146:149], v[202:205], v[76:79]
	v_mfma_f32_16x16x32_bf16 v[72:75], v[154:157], v[202:205], v[72:75]
	s_setprio 0
	s_setprio 1
	v_mfma_f32_16x16x32_bf16 v[116:119], v[158:161], v[174:177], v[116:119]
	v_mfma_f32_16x16x32_bf16 v[112:115], v[166:169], v[174:177], v[112:115]
	v_mfma_f32_16x16x32_bf16 v[100:103], v[158:161], v[182:185], v[100:103]
	v_mfma_f32_16x16x32_bf16 v[96:99], v[166:169], v[182:185], v[96:99]
	v_mfma_f32_16x16x32_bf16 v[84:87], v[158:161], v[190:193], v[84:87]
	v_mfma_f32_16x16x32_bf16 v[80:83], v[166:169], v[190:193], v[80:83]
	v_mfma_f32_16x16x32_bf16 v[68:71], v[158:161], v[198:201], v[68:71]
	v_mfma_f32_16x16x32_bf16 v[64:67], v[166:169], v[198:201], v[64:67]
	v_mfma_f32_16x16x32_bf16 v[116:119], v[162:165], v[178:181], v[116:119]
	v_mfma_f32_16x16x32_bf16 v[112:115], v[170:173], v[178:181], v[112:115]
	v_mfma_f32_16x16x32_bf16 v[100:103], v[162:165], v[186:189], v[100:103]
	v_mfma_f32_16x16x32_bf16 v[96:99], v[170:173], v[186:189], v[96:99]
	v_mfma_f32_16x16x32_bf16 v[84:87], v[162:165], v[194:197], v[84:87]
	v_mfma_f32_16x16x32_bf16 v[80:83], v[170:173], v[194:197], v[80:83]
	v_mfma_f32_16x16x32_bf16 v[68:71], v[162:165], v[202:205], v[68:71]
	v_mfma_f32_16x16x32_bf16 v[64:67], v[170:173], v[202:205], v[64:67]
	s_setprio 0
	s_cselect_b32 s45, s29, s71
	s_cselect_b32 s44, s28, s70
	s_add_i32 s77, s59, s48
	s_barrier
	v_mov_b32_e32 v206, v139
	v_mov_b32_e32 v207, v138
	s_mov_b64 s[78:79], s[40:41]
	s_mov_b32 m0, s77
	ds_read_b128 v[174:177], v143 offset:16384
	ds_read_b128 v[178:181], v143 offset:17408
	ds_read_b128 v[182:185], v143 offset:18432
	ds_read_b128 v[186:189], v143 offset:19456
	ds_read_b128 v[190:193], v143 offset:20480
	ds_read_b128 v[194:197], v143 offset:21504
	ds_read_b128 v[198:201], v143 offset:22528
	ds_read_b128 v[202:205], v143 offset:23552
	s_nop 0
	global_load_lds_dwordx4 v207, s[78:79] nt
	s_add_i32 m0, s77, 0x2000
	s_add_i32 s77, s60, s48
	global_load_lds_dwordx4 v206, s[78:79] nt
	v_mov_b32_e32 v206, v139
	s_mov_b64 s[78:79], s[44:45]
	v_mov_b32_e32 v207, v138
	s_mov_b32 m0, s77
	s_nop 0
	global_load_lds_dwordx4 v207, s[78:79] nt
	s_add_i32 m0, s77, 0x2000
	v_mov_b32_e32 v207, v130
	global_load_lds_dwordx4 v206, s[78:79] nt
	v_mov_b32_e32 v206, v128
	s_mov_b64 s[78:79], s[38:39]
	s_mov_b32 m0, s49
	s_nop 0
	global_load_lds_dwordx4 v206, s[78:79] nt
	s_mov_b32 m0, s50
	s_nop 0
	global_load_lds_dwordx4 v207, s[78:79] nt
	s_waitcnt vmcnt(8)
	s_waitcnt lgkmcnt(0)
	s_barrier
	s_setprio 1
	v_mfma_f32_16x16x32_bf16 v[60:63], v[134:137], v[174:177], v[60:63]
	v_mfma_f32_16x16x32_bf16 v[56:59], v[150:153], v[174:177], v[56:59]
	v_mfma_f32_16x16x32_bf16 v[44:47], v[134:137], v[182:185], v[44:47]
	v_mfma_f32_16x16x32_bf16 v[40:43], v[150:153], v[182:185], v[40:43]
	v_mfma_f32_16x16x32_bf16 v[28:31], v[134:137], v[190:193], v[28:31]
	v_mfma_f32_16x16x32_bf16 v[24:27], v[150:153], v[190:193], v[24:27]
	v_mfma_f32_16x16x32_bf16 v[12:15], v[134:137], v[198:201], v[12:15]
	v_mfma_f32_16x16x32_bf16 v[8:11], v[150:153], v[198:201], v[8:11]
	v_mfma_f32_16x16x32_bf16 v[60:63], v[146:149], v[178:181], v[60:63]
	v_mfma_f32_16x16x32_bf16 v[56:59], v[154:157], v[178:181], v[56:59]
	v_mfma_f32_16x16x32_bf16 v[44:47], v[146:149], v[186:189], v[44:47]
	v_mfma_f32_16x16x32_bf16 v[40:43], v[154:157], v[186:189], v[40:43]
	v_mfma_f32_16x16x32_bf16 v[28:31], v[146:149], v[194:197], v[28:31]
	v_mfma_f32_16x16x32_bf16 v[24:27], v[154:157], v[194:197], v[24:27]
	v_mfma_f32_16x16x32_bf16 v[12:15], v[146:149], v[202:205], v[12:15]
	v_mfma_f32_16x16x32_bf16 v[8:11], v[154:157], v[202:205], v[8:11]
	s_setprio 0
	s_setprio 1
	v_mfma_f32_16x16x32_bf16 v[52:55], v[158:161], v[174:177], v[52:55]
	v_mfma_f32_16x16x32_bf16 v[48:51], v[166:169], v[174:177], v[48:51]
	v_mfma_f32_16x16x32_bf16 v[36:39], v[158:161], v[182:185], v[36:39]
	v_mfma_f32_16x16x32_bf16 v[32:35], v[166:169], v[182:185], v[32:35]
	v_mfma_f32_16x16x32_bf16 v[20:23], v[158:161], v[190:193], v[20:23]
	v_mfma_f32_16x16x32_bf16 v[16:19], v[166:169], v[190:193], v[16:19]
	v_mfma_f32_16x16x32_bf16 v[4:7], v[158:161], v[198:201], v[4:7]
	v_mfma_f32_16x16x32_bf16 v[0:3], v[166:169], v[198:201], v[0:3]
	v_mfma_f32_16x16x32_bf16 v[52:55], v[162:165], v[178:181], v[52:55]
	v_mfma_f32_16x16x32_bf16 v[48:51], v[170:173], v[178:181], v[48:51]
	v_mfma_f32_16x16x32_bf16 v[36:39], v[162:165], v[186:189], v[36:39]
	v_mfma_f32_16x16x32_bf16 v[32:35], v[170:173], v[186:189], v[32:35]
	v_mfma_f32_16x16x32_bf16 v[20:23], v[162:165], v[194:197], v[20:23]
	v_mfma_f32_16x16x32_bf16 v[16:19], v[170:173], v[194:197], v[16:19]
	v_mfma_f32_16x16x32_bf16 v[4:7], v[162:165], v[202:205], v[4:7]
	v_mfma_f32_16x16x32_bf16 v[0:3], v[170:173], v[202:205], v[0:3]
	s_setprio 0
	s_add_i32 s77, 0, 0x18000
	s_add_i32 s78, 0, 0x1c000
	s_barrier
	v_add_u32_e32 v154, s77, v131
	v_add_u32_e32 v170, s78, v131
	ds_read_b128 v[134:137], v154
	ds_read_b128 v[146:149], v154 offset:1024
	ds_read_b128 v[150:153], v154 offset:2048
	ds_read_b128 v[154:157], v154 offset:3072
	ds_read_b128 v[158:161], v170
	ds_read_b128 v[162:165], v170 offset:1024
	ds_read_b128 v[166:169], v170 offset:2048
	ds_read_b128 v[170:173], v170 offset:3072
	v_mov_b32_e32 v206, v128
	v_mov_b32_e32 v207, v130
	s_mov_b32 m0, s51
	ds_read_b128 v[174:177], v143 offset:32768
	ds_read_b128 v[178:181], v143 offset:33792
	ds_read_b128 v[182:185], v143 offset:34816
	ds_read_b128 v[186:189], v143 offset:35840
	ds_read_b128 v[190:193], v143 offset:36864
	ds_read_b128 v[194:197], v143 offset:37888
	ds_read_b128 v[198:201], v143 offset:38912
	ds_read_b128 v[202:205], v143 offset:39936
	s_nop 0
	global_load_lds_dwordx4 v206, s[42:43] nt
	s_mov_b32 m0, s52
	s_nop 0
	global_load_lds_dwordx4 v207, s[42:43] nt
	s_waitcnt vmcnt(8)
	s_waitcnt lgkmcnt(0)
	s_barrier
	s_setprio 1
	v_mfma_f32_16x16x32_bf16 v[124:127], v[134:137], v[174:177], v[124:127]
	v_mfma_f32_16x16x32_bf16 v[120:123], v[150:153], v[174:177], v[120:123]
	v_mfma_f32_16x16x32_bf16 v[108:111], v[134:137], v[182:185], v[108:111]
	v_mfma_f32_16x16x32_bf16 v[104:107], v[150:153], v[182:185], v[104:107]
	v_mfma_f32_16x16x32_bf16 v[92:95], v[134:137], v[190:193], v[92:95]
	v_mfma_f32_16x16x32_bf16 v[88:91], v[150:153], v[190:193], v[88:91]
	v_mfma_f32_16x16x32_bf16 v[76:79], v[134:137], v[198:201], v[76:79]
	v_mfma_f32_16x16x32_bf16 v[72:75], v[150:153], v[198:201], v[72:75]
	v_mfma_f32_16x16x32_bf16 v[124:127], v[146:149], v[178:181], v[124:127]
	v_mfma_f32_16x16x32_bf16 v[120:123], v[154:157], v[178:181], v[120:123]
	v_mfma_f32_16x16x32_bf16 v[108:111], v[146:149], v[186:189], v[108:111]
	v_mfma_f32_16x16x32_bf16 v[104:107], v[154:157], v[186:189], v[104:107]
	v_mfma_f32_16x16x32_bf16 v[92:95], v[146:149], v[194:197], v[92:95]
	v_mfma_f32_16x16x32_bf16 v[88:91], v[154:157], v[194:197], v[88:91]
	v_mfma_f32_16x16x32_bf16 v[76:79], v[146:149], v[202:205], v[76:79]
	v_mfma_f32_16x16x32_bf16 v[72:75], v[154:157], v[202:205], v[72:75]
	s_setprio 0
	s_setprio 1
	v_mfma_f32_16x16x32_bf16 v[116:119], v[158:161], v[174:177], v[116:119]
	v_mfma_f32_16x16x32_bf16 v[112:115], v[166:169], v[174:177], v[112:115]
	v_mfma_f32_16x16x32_bf16 v[100:103], v[158:161], v[182:185], v[100:103]
	v_mfma_f32_16x16x32_bf16 v[96:99], v[166:169], v[182:185], v[96:99]
	v_mfma_f32_16x16x32_bf16 v[84:87], v[158:161], v[190:193], v[84:87]
	v_mfma_f32_16x16x32_bf16 v[80:83], v[166:169], v[190:193], v[80:83]
	v_mfma_f32_16x16x32_bf16 v[68:71], v[158:161], v[198:201], v[68:71]
	v_mfma_f32_16x16x32_bf16 v[64:67], v[166:169], v[198:201], v[64:67]
	v_mfma_f32_16x16x32_bf16 v[116:119], v[162:165], v[178:181], v[116:119]
	v_mfma_f32_16x16x32_bf16 v[112:115], v[170:173], v[178:181], v[112:115]
	v_mfma_f32_16x16x32_bf16 v[100:103], v[162:165], v[186:189], v[100:103]
	v_mfma_f32_16x16x32_bf16 v[96:99], v[170:173], v[186:189], v[96:99]
	v_mfma_f32_16x16x32_bf16 v[84:87], v[162:165], v[194:197], v[84:87]
	v_mfma_f32_16x16x32_bf16 v[80:83], v[170:173], v[194:197], v[80:83]
	v_mfma_f32_16x16x32_bf16 v[68:71], v[162:165], v[202:205], v[68:71]
	v_mfma_f32_16x16x32_bf16 v[64:67], v[170:173], v[202:205], v[64:67]
	s_setprio 0
	s_add_u32 s40, s40, 0x80
	s_addc_u32 s41, s41, 0
	s_add_i32 s42, s77, s48
	s_barrier
	v_mov_b32_e32 v206, v139
	v_mov_b32_e32 v207, v138
	s_mov_b32 m0, s42
	ds_read_b128 v[174:177], v143 offset:49152
	ds_read_b128 v[178:181], v143 offset:50176
	ds_read_b128 v[182:185], v143 offset:51200
	ds_read_b128 v[186:189], v143 offset:52224
	ds_read_b128 v[190:193], v143 offset:53248
	ds_read_b128 v[194:197], v143 offset:54272
	ds_read_b128 v[198:201], v143 offset:55296
	ds_read_b128 v[202:205], v143 offset:56320
	s_nop 0
	global_load_lds_dwordx4 v207, s[40:41] nt
	s_add_i32 m0, s42, 0x2000
	v_mov_b32_e32 v207, v138
	global_load_lds_dwordx4 v206, s[40:41] nt
	s_add_u32 s40, s44, 0x80
	s_addc_u32 s41, s45, 0
	s_add_i32 s42, s78, s48
	v_mov_b32_e32 v206, v139
	s_mov_b32 m0, s42
	s_nop 0
	global_load_lds_dwordx4 v207, s[40:41] nt
	s_add_i32 m0, s42, 0x2000
	s_add_u32 s38, s38, 0x80
	global_load_lds_dwordx4 v206, s[40:41] nt
	s_addc_u32 s39, s39, 0
	v_mov_b32_e32 v206, v128
	v_mov_b32_e32 v207, v130
	s_mov_b32 m0, s56
	s_nop 0
	global_load_lds_dwordx4 v206, s[38:39] nt
	s_mov_b32 m0, s57
	s_nop 0
	global_load_lds_dwordx4 v207, s[38:39] nt
	s_waitcnt vmcnt(8)
	s_waitcnt lgkmcnt(0)
	s_barrier
	s_setprio 1
	v_mfma_f32_16x16x32_bf16 v[60:63], v[134:137], v[174:177], v[60:63]
	v_mfma_f32_16x16x32_bf16 v[56:59], v[150:153], v[174:177], v[56:59]
	v_mfma_f32_16x16x32_bf16 v[44:47], v[134:137], v[182:185], v[44:47]
	v_mfma_f32_16x16x32_bf16 v[40:43], v[150:153], v[182:185], v[40:43]
	v_mfma_f32_16x16x32_bf16 v[28:31], v[134:137], v[190:193], v[28:31]
	v_mfma_f32_16x16x32_bf16 v[24:27], v[150:153], v[190:193], v[24:27]
	v_mfma_f32_16x16x32_bf16 v[12:15], v[134:137], v[198:201], v[12:15]
	v_mfma_f32_16x16x32_bf16 v[8:11], v[150:153], v[198:201], v[8:11]
	v_mfma_f32_16x16x32_bf16 v[60:63], v[146:149], v[178:181], v[60:63]
	v_mfma_f32_16x16x32_bf16 v[56:59], v[154:157], v[178:181], v[56:59]
	v_mfma_f32_16x16x32_bf16 v[44:47], v[146:149], v[186:189], v[44:47]
	v_mfma_f32_16x16x32_bf16 v[40:43], v[154:157], v[186:189], v[40:43]
	v_mfma_f32_16x16x32_bf16 v[28:31], v[146:149], v[194:197], v[28:31]
	v_mfma_f32_16x16x32_bf16 v[24:27], v[154:157], v[194:197], v[24:27]
	v_mfma_f32_16x16x32_bf16 v[12:15], v[146:149], v[202:205], v[12:15]
	v_mfma_f32_16x16x32_bf16 v[8:11], v[154:157], v[202:205], v[8:11]
	s_setprio 0
	s_setprio 1
	v_mfma_f32_16x16x32_bf16 v[52:55], v[158:161], v[174:177], v[52:55]
	v_mfma_f32_16x16x32_bf16 v[48:51], v[166:169], v[174:177], v[48:51]
	v_mfma_f32_16x16x32_bf16 v[36:39], v[158:161], v[182:185], v[36:39]
	v_mfma_f32_16x16x32_bf16 v[32:35], v[166:169], v[182:185], v[32:35]
	v_mfma_f32_16x16x32_bf16 v[20:23], v[158:161], v[190:193], v[20:23]
	v_mfma_f32_16x16x32_bf16 v[16:19], v[166:169], v[190:193], v[16:19]
	v_mfma_f32_16x16x32_bf16 v[4:7], v[158:161], v[198:201], v[4:7]
	v_mfma_f32_16x16x32_bf16 v[0:3], v[166:169], v[198:201], v[0:3]
	v_mfma_f32_16x16x32_bf16 v[52:55], v[162:165], v[178:181], v[52:55]
	v_mfma_f32_16x16x32_bf16 v[48:51], v[170:173], v[178:181], v[48:51]
	v_mfma_f32_16x16x32_bf16 v[36:39], v[162:165], v[186:189], v[36:39]
	v_mfma_f32_16x16x32_bf16 v[32:35], v[170:173], v[186:189], v[32:35]
	v_mfma_f32_16x16x32_bf16 v[20:23], v[162:165], v[194:197], v[20:23]
	v_mfma_f32_16x16x32_bf16 v[16:19], v[170:173], v[194:197], v[16:19]
	v_mfma_f32_16x16x32_bf16 v[4:7], v[162:165], v[202:205], v[4:7]
	v_mfma_f32_16x16x32_bf16 v[0:3], v[170:173], v[202:205], v[0:3]
	s_setprio 0
	s_add_u32 s68, s68, 0x100
	s_addc_u32 s69, s69, 0
	s_add_u32 s70, s70, 0x100
	s_addc_u32 s71, s71, 0
	s_add_u32 s72, s72, 0x100
	s_addc_u32 s73, s73, 0
	s_add_u32 s74, s74, 0x100
	s_addc_u32 s75, s75, 0
	s_cmp_ge_i32 s76, s3
	s_mov_b32 s38, s76
	s_barrier
	s_cbranch_scc0 .LBB0_1223
	s_and_b64 vcc, exec, s[12:13]
	s_cbranch_vccz .LBB0_1226

.LBB0_1252:
	ds_read_b128 v[140:143], v137
	ds_read_b128 v[144:147], v137 offset:1024
	ds_read_b128 v[148:151], v137 offset:2048
	ds_read_b128 v[152:155], v137 offset:3072
	ds_read_b128 v[156:159], v138
	ds_read_b128 v[160:163], v138 offset:1024
	ds_read_b128 v[164:167], v138 offset:2048
	ds_read_b128 v[168:171], v138 offset:3072
	s_add_i32 s73, s38, 2
	s_add_u32 s44, s71, 0xffffff80
	s_addc_u32 s45, s72, -1
	s_add_i32 m0, s48, 0xc000
	s_add_i32 s74, s48, 0xe000
	s_cmp_eq_u32 s62, s38
	s_cselect_b32 s38, s36, s69
	s_cselect_b32 s39, s37, s70
	s_cselect_b32 s41, s35, s66
	s_cselect_b32 s40, s34, s65
	s_cselect_b32 s43, s29, s72
	s_cselect_b32 s42, s28, s71
	v_mov_b32_e32 v204, v130
	v_mov_b32_e32 v205, v128
	ds_read_b128 v[172:175], v139
	ds_read_b128 v[176:179], v139 offset:1024
	ds_read_b128 v[180:183], v139 offset:2048
	ds_read_b128 v[184:187], v139 offset:3072
	ds_read_b128 v[188:191], v139 offset:4096
	ds_read_b128 v[192:195], v139 offset:5120
	ds_read_b128 v[196:199], v139 offset:6144
	ds_read_b128 v[200:203], v139 offset:7168
	s_nop 0
	global_load_lds_dwordx4 v205, s[44:45] nt
	s_mov_b32 m0, s74
	s_nop 0
	global_load_lds_dwordx4 v204, s[44:45] nt
	s_waitcnt vmcnt(8)
	s_waitcnt lgkmcnt(0)
	s_barrier
	s_setprio 1
	v_mfma_f32_16x16x32_bf16 v[124:127], v[140:143], v[172:175], v[124:127]
	v_mfma_f32_16x16x32_bf16 v[120:123], v[148:151], v[172:175], v[120:123]
	v_mfma_f32_16x16x32_bf16 v[108:111], v[140:143], v[180:183], v[108:111]
	v_mfma_f32_16x16x32_bf16 v[104:107], v[148:151], v[180:183], v[104:107]
	v_mfma_f32_16x16x32_bf16 v[92:95], v[140:143], v[188:191], v[92:95]
	v_mfma_f32_16x16x32_bf16 v[88:91], v[148:151], v[188:191], v[88:91]
	v_mfma_f32_16x16x32_bf16 v[76:79], v[140:143], v[196:199], v[76:79]
	v_mfma_f32_16x16x32_bf16 v[72:75], v[148:151], v[196:199], v[72:75]
	v_mfma_f32_16x16x32_bf16 v[124:127], v[144:147], v[176:179], v[124:127]
	v_mfma_f32_16x16x32_bf16 v[120:123], v[152:155], v[176:179], v[120:123]
	v_mfma_f32_16x16x32_bf16 v[108:111], v[144:147], v[184:187], v[108:111]
	v_mfma_f32_16x16x32_bf16 v[104:107], v[152:155], v[184:187], v[104:107]
	v_mfma_f32_16x16x32_bf16 v[92:95], v[144:147], v[192:195], v[92:95]
	v_mfma_f32_16x16x32_bf16 v[88:91], v[152:155], v[192:195], v[88:91]
	v_mfma_f32_16x16x32_bf16 v[76:79], v[144:147], v[200:203], v[76:79]
	v_mfma_f32_16x16x32_bf16 v[72:75], v[152:155], v[200:203], v[72:75]
	s_setprio 0
	s_setprio 1
	v_mfma_f32_16x16x32_bf16 v[116:119], v[156:159], v[172:175], v[116:119]
	v_mfma_f32_16x16x32_bf16 v[112:115], v[164:167], v[172:175], v[112:115]
	v_mfma_f32_16x16x32_bf16 v[100:103], v[156:159], v[180:183], v[100:103]
	v_mfma_f32_16x16x32_bf16 v[96:99], v[164:167], v[180:183], v[96:99]
	v_mfma_f32_16x16x32_bf16 v[84:87], v[156:159], v[188:191], v[84:87]
	v_mfma_f32_16x16x32_bf16 v[80:83], v[164:167], v[188:191], v[80:83]
	v_mfma_f32_16x16x32_bf16 v[68:71], v[156:159], v[196:199], v[68:71]
	v_mfma_f32_16x16x32_bf16 v[60:63], v[164:167], v[196:199], v[60:63]
	v_mfma_f32_16x16x32_bf16 v[116:119], v[160:163], v[176:179], v[116:119]
	v_mfma_f32_16x16x32_bf16 v[112:115], v[168:171], v[176:179], v[112:115]
	v_mfma_f32_16x16x32_bf16 v[100:103], v[160:163], v[184:187], v[100:103]
	v_mfma_f32_16x16x32_bf16 v[96:99], v[168:171], v[184:187], v[96:99]
	v_mfma_f32_16x16x32_bf16 v[84:87], v[160:163], v[192:195], v[84:87]
	v_mfma_f32_16x16x32_bf16 v[80:83], v[168:171], v[192:195], v[80:83]
	v_mfma_f32_16x16x32_bf16 v[68:71], v[160:163], v[200:203], v[68:71]
	v_mfma_f32_16x16x32_bf16 v[60:63], v[168:171], v[200:203], v[60:63]
	s_setprio 0
	s_cselect_b32 s45, s31, s68
	s_cselect_b32 s44, s30, s67
	s_add_i32 s76, s63, s33
	s_barrier
	s_mov_b64 s[74:75], s[40:41]
	s_mov_b32 m0, s76
	ds_read_b128 v[172:175], v139 offset:16384
	ds_read_b128 v[176:179], v139 offset:17408
	ds_read_b128 v[180:183], v139 offset:18432
	ds_read_b128 v[184:187], v139 offset:19456
	ds_read_b128 v[188:191], v139 offset:20480
	ds_read_b128 v[192:195], v139 offset:21504
	ds_read_b128 v[196:199], v139 offset:22528
	ds_read_b128 v[200:203], v139 offset:23552
	s_nop 0
	global_load_lds_dwordx4 v134, s[74:75]
	s_add_i32 m0, s76, 0x2000
	s_add_i32 s76, s64, s33
	global_load_lds_dwordx4 v135, s[74:75]
	s_mov_b64 s[74:75], s[44:45]
	s_mov_b32 m0, s76
	s_nop 0
	global_load_lds_dwordx4 v134, s[74:75]
	s_add_i32 m0, s76, 0x2000
	v_mov_b32_e32 v204, v130
	global_load_lds_dwordx4 v135, s[74:75]
	s_mov_b64 s[74:75], s[38:39]
	v_mov_b32_e32 v205, v128
	s_mov_b32 m0, s48
	s_nop 0
	global_load_lds_dwordx4 v205, s[74:75] nt
	s_mov_b32 m0, s49
	s_nop 0
	global_load_lds_dwordx4 v204, s[74:75] nt
	s_waitcnt vmcnt(8)
	s_waitcnt lgkmcnt(0)
	s_barrier
	s_setprio 1
	v_mfma_f32_16x16x32_bf16 v[64:67], v[140:143], v[172:175], v[64:67]
	v_mfma_f32_16x16x32_bf16 v[56:59], v[148:151], v[172:175], v[56:59]
	v_mfma_f32_16x16x32_bf16 v[44:47], v[140:143], v[180:183], v[44:47]
	v_mfma_f32_16x16x32_bf16 v[40:43], v[148:151], v[180:183], v[40:43]
	v_mfma_f32_16x16x32_bf16 v[28:31], v[140:143], v[188:191], v[28:31]
	v_mfma_f32_16x16x32_bf16 v[24:27], v[148:151], v[188:191], v[24:27]
	v_mfma_f32_16x16x32_bf16 v[12:15], v[140:143], v[196:199], v[12:15]
	v_mfma_f32_16x16x32_bf16 v[8:11], v[148:151], v[196:199], v[8:11]
	v_mfma_f32_16x16x32_bf16 v[64:67], v[144:147], v[176:179], v[64:67]
	v_mfma_f32_16x16x32_bf16 v[56:59], v[152:155], v[176:179], v[56:59]
	v_mfma_f32_16x16x32_bf16 v[44:47], v[144:147], v[184:187], v[44:47]
	v_mfma_f32_16x16x32_bf16 v[40:43], v[152:155], v[184:187], v[40:43]
	v_mfma_f32_16x16x32_bf16 v[28:31], v[144:147], v[192:195], v[28:31]
	v_mfma_f32_16x16x32_bf16 v[24:27], v[152:155], v[192:195], v[24:27]
	v_mfma_f32_16x16x32_bf16 v[12:15], v[144:147], v[200:203], v[12:15]
	v_mfma_f32_16x16x32_bf16 v[8:11], v[152:155], v[200:203], v[8:11]
	s_setprio 0
	s_setprio 1
	v_mfma_f32_16x16x32_bf16 v[52:55], v[156:159], v[172:175], v[52:55]
	v_mfma_f32_16x16x32_bf16 v[48:51], v[164:167], v[172:175], v[48:51]
	v_mfma_f32_16x16x32_bf16 v[36:39], v[156:159], v[180:183], v[36:39]
	v_mfma_f32_16x16x32_bf16 v[32:35], v[164:167], v[180:183], v[32:35]
	v_mfma_f32_16x16x32_bf16 v[20:23], v[156:159], v[188:191], v[20:23]
	v_mfma_f32_16x16x32_bf16 v[16:19], v[164:167], v[188:191], v[16:19]
	v_mfma_f32_16x16x32_bf16 v[4:7], v[156:159], v[196:199], v[4:7]
	v_mfma_f32_16x16x32_bf16 v[0:3], v[164:167], v[196:199], v[0:3]
	v_mfma_f32_16x16x32_bf16 v[52:55], v[160:163], v[176:179], v[52:55]
	v_mfma_f32_16x16x32_bf16 v[48:51], v[168:171], v[176:179], v[48:51]
	v_mfma_f32_16x16x32_bf16 v[36:39], v[160:163], v[184:187], v[36:39]
	v_mfma_f32_16x16x32_bf16 v[32:35], v[168:171], v[184:187], v[32:35]
	v_mfma_f32_16x16x32_bf16 v[20:23], v[160:163], v[192:195], v[20:23]
	v_mfma_f32_16x16x32_bf16 v[16:19], v[168:171], v[192:195], v[16:19]
	v_mfma_f32_16x16x32_bf16 v[4:7], v[160:163], v[200:203], v[4:7]
	v_mfma_f32_16x16x32_bf16 v[0:3], v[168:171], v[200:203], v[0:3]
	s_setprio 0
	s_add_i32 s74, 0, 0x18000
	s_add_i32 s75, 0, 0x1c000
	s_barrier
	v_add_u32_e32 v152, s74, v131
	v_add_u32_e32 v168, s75, v131
	ds_read_b128 v[140:143], v152
	ds_read_b128 v[144:147], v152 offset:1024
	ds_read_b128 v[148:151], v152 offset:2048
	ds_read_b128 v[152:155], v152 offset:3072
	ds_read_b128 v[156:159], v168
	ds_read_b128 v[160:163], v168 offset:1024
	ds_read_b128 v[164:167], v168 offset:2048
	ds_read_b128 v[168:171], v168 offset:3072
	v_mov_b32_e32 v204, v130
	v_mov_b32_e32 v205, v128
	s_mov_b32 m0, s50
	ds_read_b128 v[172:175], v139 offset:32768
	ds_read_b128 v[176:179], v139 offset:33792
	ds_read_b128 v[180:183], v139 offset:34816
	ds_read_b128 v[184:187], v139 offset:35840
	ds_read_b128 v[188:191], v139 offset:36864
	ds_read_b128 v[192:195], v139 offset:37888
	ds_read_b128 v[196:199], v139 offset:38912
	ds_read_b128 v[200:203], v139 offset:39936
	s_nop 0
	global_load_lds_dwordx4 v205, s[42:43] nt
	s_mov_b32 m0, s51
	s_nop 0
	global_load_lds_dwordx4 v204, s[42:43] nt
	s_waitcnt vmcnt(8)
	s_waitcnt lgkmcnt(0)
	s_barrier
	s_setprio 1
	v_mfma_f32_16x16x32_bf16 v[124:127], v[140:143], v[172:175], v[124:127]
	v_mfma_f32_16x16x32_bf16 v[120:123], v[148:151], v[172:175], v[120:123]
	v_mfma_f32_16x16x32_bf16 v[108:111], v[140:143], v[180:183], v[108:111]
	v_mfma_f32_16x16x32_bf16 v[104:107], v[148:151], v[180:183], v[104:107]
	v_mfma_f32_16x16x32_bf16 v[92:95], v[140:143], v[188:191], v[92:95]
	v_mfma_f32_16x16x32_bf16 v[88:91], v[148:151], v[188:191], v[88:91]
	v_mfma_f32_16x16x32_bf16 v[76:79], v[140:143], v[196:199], v[76:79]
	v_mfma_f32_16x16x32_bf16 v[72:75], v[148:151], v[196:199], v[72:75]
	v_mfma_f32_16x16x32_bf16 v[124:127], v[144:147], v[176:179], v[124:127]
	v_mfma_f32_16x16x32_bf16 v[120:123], v[152:155], v[176:179], v[120:123]
	v_mfma_f32_16x16x32_bf16 v[108:111], v[144:147], v[184:187], v[108:111]
	v_mfma_f32_16x16x32_bf16 v[104:107], v[152:155], v[184:187], v[104:107]
	v_mfma_f32_16x16x32_bf16 v[92:95], v[144:147], v[192:195], v[92:95]
	v_mfma_f32_16x16x32_bf16 v[88:91], v[152:155], v[192:195], v[88:91]
	v_mfma_f32_16x16x32_bf16 v[76:79], v[144:147], v[200:203], v[76:79]
	v_mfma_f32_16x16x32_bf16 v[72:75], v[152:155], v[200:203], v[72:75]
	s_setprio 0
	s_setprio 1
	v_mfma_f32_16x16x32_bf16 v[116:119], v[156:159], v[172:175], v[116:119]
	v_mfma_f32_16x16x32_bf16 v[112:115], v[164:167], v[172:175], v[112:115]
	v_mfma_f32_16x16x32_bf16 v[100:103], v[156:159], v[180:183], v[100:103]
	v_mfma_f32_16x16x32_bf16 v[96:99], v[164:167], v[180:183], v[96:99]
	v_mfma_f32_16x16x32_bf16 v[84:87], v[156:159], v[188:191], v[84:87]
	v_mfma_f32_16x16x32_bf16 v[80:83], v[164:167], v[188:191], v[80:83]
	v_mfma_f32_16x16x32_bf16 v[68:71], v[156:159], v[196:199], v[68:71]
	v_mfma_f32_16x16x32_bf16 v[60:63], v[164:167], v[196:199], v[60:63]
	v_mfma_f32_16x16x32_bf16 v[116:119], v[160:163], v[176:179], v[116:119]
	v_mfma_f32_16x16x32_bf16 v[112:115], v[168:171], v[176:179], v[112:115]
	v_mfma_f32_16x16x32_bf16 v[100:103], v[160:163], v[184:187], v[100:103]
	v_mfma_f32_16x16x32_bf16 v[96:99], v[168:171], v[184:187], v[96:99]
	v_mfma_f32_16x16x32_bf16 v[84:87], v[160:163], v[192:195], v[84:87]
	v_mfma_f32_16x16x32_bf16 v[80:83], v[168:171], v[192:195], v[80:83]
	v_mfma_f32_16x16x32_bf16 v[68:71], v[160:163], v[200:203], v[68:71]
	v_mfma_f32_16x16x32_bf16 v[60:63], v[168:171], v[200:203], v[60:63]
	s_setprio 0
	s_add_u32 s40, s40, 0x80
	s_addc_u32 s41, s41, 0
	s_add_i32 s42, s74, s33
	s_barrier
	s_mov_b32 m0, s42
	ds_read_b128 v[172:175], v139 offset:49152
	ds_read_b128 v[176:179], v139 offset:50176
	ds_read_b128 v[180:183], v139 offset:51200
	ds_read_b128 v[184:187], v139 offset:52224
	ds_read_b128 v[188:191], v139 offset:53248
	ds_read_b128 v[192:195], v139 offset:54272
	ds_read_b128 v[196:199], v139 offset:55296
	ds_read_b128 v[200:203], v139 offset:56320
	s_nop 0
	global_load_lds_dwordx4 v134, s[40:41]
	s_add_i32 m0, s42, 0x2000
	s_nop 0
	global_load_lds_dwordx4 v135, s[40:41]
	s_add_u32 s40, s44, 0x80
	s_addc_u32 s41, s45, 0
	s_add_i32 s42, s75, s33
	s_mov_b32 m0, s42
	s_nop 0
	global_load_lds_dwordx4 v134, s[40:41]
	s_add_i32 m0, s42, 0x2000
	s_add_u32 s38, s38, 0x80
	global_load_lds_dwordx4 v135, s[40:41]
	s_addc_u32 s39, s39, 0
	v_mov_b32_e32 v204, v130
	v_mov_b32_e32 v205, v128
	s_mov_b32 m0, s60
	s_nop 0
	global_load_lds_dwordx4 v205, s[38:39] nt
	s_mov_b32 m0, s61
	s_nop 0
	global_load_lds_dwordx4 v204, s[38:39] nt
	s_waitcnt vmcnt(8)
	s_waitcnt lgkmcnt(0)
	s_barrier
	s_setprio 1
	v_mfma_f32_16x16x32_bf16 v[64:67], v[140:143], v[172:175], v[64:67]
	v_mfma_f32_16x16x32_bf16 v[56:59], v[148:151], v[172:175], v[56:59]
	v_mfma_f32_16x16x32_bf16 v[44:47], v[140:143], v[180:183], v[44:47]
	v_mfma_f32_16x16x32_bf16 v[40:43], v[148:151], v[180:183], v[40:43]
	v_mfma_f32_16x16x32_bf16 v[28:31], v[140:143], v[188:191], v[28:31]
	v_mfma_f32_16x16x32_bf16 v[24:27], v[148:151], v[188:191], v[24:27]
	v_mfma_f32_16x16x32_bf16 v[12:15], v[140:143], v[196:199], v[12:15]
	v_mfma_f32_16x16x32_bf16 v[8:11], v[148:151], v[196:199], v[8:11]
	v_mfma_f32_16x16x32_bf16 v[64:67], v[144:147], v[176:179], v[64:67]
	v_mfma_f32_16x16x32_bf16 v[56:59], v[152:155], v[176:179], v[56:59]
	v_mfma_f32_16x16x32_bf16 v[44:47], v[144:147], v[184:187], v[44:47]
	v_mfma_f32_16x16x32_bf16 v[40:43], v[152:155], v[184:187], v[40:43]
	v_mfma_f32_16x16x32_bf16 v[28:31], v[144:147], v[192:195], v[28:31]
	v_mfma_f32_16x16x32_bf16 v[24:27], v[152:155], v[192:195], v[24:27]
	v_mfma_f32_16x16x32_bf16 v[12:15], v[144:147], v[200:203], v[12:15]
	v_mfma_f32_16x16x32_bf16 v[8:11], v[152:155], v[200:203], v[8:11]
	s_setprio 0
	s_setprio 1
	v_mfma_f32_16x16x32_bf16 v[52:55], v[156:159], v[172:175], v[52:55]
	v_mfma_f32_16x16x32_bf16 v[48:51], v[164:167], v[172:175], v[48:51]
	v_mfma_f32_16x16x32_bf16 v[36:39], v[156:159], v[180:183], v[36:39]
	v_mfma_f32_16x16x32_bf16 v[32:35], v[164:167], v[180:183], v[32:35]
	v_mfma_f32_16x16x32_bf16 v[20:23], v[156:159], v[188:191], v[20:23]
	v_mfma_f32_16x16x32_bf16 v[16:19], v[164:167], v[188:191], v[16:19]
	v_mfma_f32_16x16x32_bf16 v[4:7], v[156:159], v[196:199], v[4:7]
	v_mfma_f32_16x16x32_bf16 v[0:3], v[164:167], v[196:199], v[0:3]
	v_mfma_f32_16x16x32_bf16 v[52:55], v[160:163], v[176:179], v[52:55]
	v_mfma_f32_16x16x32_bf16 v[48:51], v[168:171], v[176:179], v[48:51]
	v_mfma_f32_16x16x32_bf16 v[36:39], v[160:163], v[184:187], v[36:39]
	v_mfma_f32_16x16x32_bf16 v[32:35], v[168:171], v[184:187], v[32:35]
	v_mfma_f32_16x16x32_bf16 v[20:23], v[160:163], v[192:195], v[20:23]
	v_mfma_f32_16x16x32_bf16 v[16:19], v[168:171], v[192:195], v[16:19]
	v_mfma_f32_16x16x32_bf16 v[4:7], v[160:163], v[200:203], v[4:7]
	v_mfma_f32_16x16x32_bf16 v[0:3], v[168:171], v[200:203], v[0:3]
	s_setprio 0
	s_add_u32 s65, s65, 0x100
	s_addc_u32 s66, s66, 0
	s_add_u32 s67, s67, 0x100
	s_addc_u32 s68, s68, 0
	s_add_u32 s69, s69, 0x100
	s_addc_u32 s70, s70, 0
	s_add_u32 s71, s71, 0x100
	s_addc_u32 s72, s72, 0
	s_cmp_ge_i32 s73, s2
	s_mov_b32 s38, s73
	s_barrier
	s_cbranch_scc0 .LBB0_1252
	s_and_b64 vcc, exec, s[12:13]
	s_cbranch_vccz .LBB0_1255

.LBB0_1281:
	ds_read_b128 v[96:99], v189
	ds_read_b128 v[116:119], v189 offset:1024
	ds_read_b128 v[136:139], v189 offset:2048
	ds_read_b128 v[140:143], v189 offset:3072
	ds_read_b128 v[144:147], v190
	ds_read_b128 v[148:151], v190 offset:1024
	ds_read_b128 v[152:155], v190 offset:2048
	ds_read_b128 v[158:161], v190 offset:3072
	s_add_i32 s86, s52, 2
	s_add_u32 s58, s84, 0xffffff80
	s_addc_u32 s59, s85, -1
	s_add_i32 m0, s33, 0xc000
	s_add_i32 s87, s33, 0xe000
	s_cmp_eq_u32 s69, s52
	s_cselect_b32 s52, s46, s82
	s_cselect_b32 s53, s47, s83
	s_cselect_b32 s55, s45, s79
	s_cselect_b32 s54, s44, s78
	s_cselect_b32 s57, s41, s85
	s_cselect_b32 s56, s40, s84
	ds_read_b128 v[162:165], v191
	ds_read_b128 v[166:169], v191 offset:1024
	ds_read_b128 v[170:173], v191 offset:2048
	ds_read_b128 v[174:177], v191 offset:3072
	ds_read_b128 v[178:181], v191 offset:4096
	ds_read_b128 v[192:195], v191 offset:5120
	ds_read_b128 v[196:199], v191 offset:6144
	ds_read_b128 v[200:203], v191 offset:7168
	s_nop 0
	global_load_lds_dwordx4 v184, s[58:59]
	s_mov_b32 m0, s87
	s_nop 0
	global_load_lds_dwordx4 v185, s[58:59]
	s_waitcnt vmcnt(8)
	s_waitcnt lgkmcnt(0)
	s_barrier
	s_setprio 1
	v_mfma_f32_16x16x32_bf16 v[132:135], v[96:99], v[162:165], v[132:135]
	v_mfma_f32_16x16x32_bf16 v[124:127], v[136:139], v[162:165], v[124:127]
	v_mfma_f32_16x16x32_bf16 v[112:115], v[96:99], v[170:173], v[112:115]
	v_mfma_f32_16x16x32_bf16 v[104:107], v[136:139], v[170:173], v[104:107]
	v_mfma_f32_16x16x32_bf16 v[92:95], v[96:99], v[178:181], v[92:95]
	v_mfma_f32_16x16x32_bf16 v[84:87], v[136:139], v[178:181], v[84:87]
	v_mfma_f32_16x16x32_bf16 v[76:79], v[96:99], v[196:199], v[76:79]
	v_mfma_f32_16x16x32_bf16 v[68:71], v[136:139], v[196:199], v[68:71]
	v_mfma_f32_16x16x32_bf16 v[132:135], v[116:119], v[166:169], v[132:135]
	v_mfma_f32_16x16x32_bf16 v[124:127], v[140:143], v[166:169], v[124:127]
	v_mfma_f32_16x16x32_bf16 v[112:115], v[116:119], v[174:177], v[112:115]
	v_mfma_f32_16x16x32_bf16 v[104:107], v[140:143], v[174:177], v[104:107]
	v_mfma_f32_16x16x32_bf16 v[92:95], v[116:119], v[192:195], v[92:95]
	v_mfma_f32_16x16x32_bf16 v[84:87], v[140:143], v[192:195], v[84:87]
	v_mfma_f32_16x16x32_bf16 v[76:79], v[116:119], v[200:203], v[76:79]
	v_mfma_f32_16x16x32_bf16 v[68:71], v[140:143], v[200:203], v[68:71]
	s_setprio 0
	s_setprio 1
	v_mfma_f32_16x16x32_bf16 v[128:131], v[144:147], v[162:165], v[128:131]
	v_mfma_f32_16x16x32_bf16 v[120:123], v[152:155], v[162:165], v[120:123]
	v_mfma_f32_16x16x32_bf16 v[108:111], v[144:147], v[170:173], v[108:111]
	v_mfma_f32_16x16x32_bf16 v[100:103], v[152:155], v[170:173], v[100:103]
	v_mfma_f32_16x16x32_bf16 v[88:91], v[144:147], v[178:181], v[88:91]
	v_mfma_f32_16x16x32_bf16 v[80:83], v[152:155], v[178:181], v[80:83]
	v_mfma_f32_16x16x32_bf16 v[72:75], v[144:147], v[196:199], v[72:75]
	v_mfma_f32_16x16x32_bf16 v[64:67], v[152:155], v[196:199], v[64:67]
	v_mfma_f32_16x16x32_bf16 v[128:131], v[148:151], v[166:169], v[128:131]
	v_mfma_f32_16x16x32_bf16 v[120:123], v[158:161], v[166:169], v[120:123]
	v_mfma_f32_16x16x32_bf16 v[108:111], v[148:151], v[174:177], v[108:111]
	v_mfma_f32_16x16x32_bf16 v[100:103], v[158:161], v[174:177], v[100:103]
	v_mfma_f32_16x16x32_bf16 v[88:91], v[148:151], v[192:195], v[88:91]
	v_mfma_f32_16x16x32_bf16 v[80:83], v[158:161], v[192:195], v[80:83]
	v_mfma_f32_16x16x32_bf16 v[72:75], v[148:151], v[200:203], v[72:75]
	v_mfma_f32_16x16x32_bf16 v[64:67], v[158:161], v[200:203], v[64:67]
	s_setprio 0
	s_cselect_b32 s59, s43, s81
	s_cselect_b32 s58, s42, s80
	s_add_i32 s87, s70, s3
	s_barrier
	s_mov_b64 s[88:89], s[54:55]
	s_mov_b32 m0, s87
	ds_read_b128 v[162:165], v191 offset:16384
	ds_read_b128 v[166:169], v191 offset:17408
	ds_read_b128 v[170:173], v191 offset:18432
	ds_read_b128 v[174:177], v191 offset:19456
	ds_read_b128 v[178:181], v191 offset:20480
	ds_read_b128 v[192:195], v191 offset:21504
	ds_read_b128 v[196:199], v191 offset:22528
	ds_read_b128 v[200:203], v191 offset:23552
	s_nop 0
	global_load_lds_dwordx4 v182, s[88:89]
	s_add_i32 m0, s87, 0x2000
	s_add_i32 s87, s71, s3
	global_load_lds_dwordx4 v183, s[88:89]
	s_mov_b64 s[88:89], s[58:59]
	s_mov_b32 m0, s87
	s_nop 0
	global_load_lds_dwordx4 v182, s[88:89]
	s_add_i32 m0, s87, 0x2000
	s_nop 0
	global_load_lds_dwordx4 v183, s[88:89]
	s_mov_b64 s[88:89], s[52:53]
	s_mov_b32 m0, s33
	s_nop 0
	global_load_lds_dwordx4 v184, s[88:89]
	s_mov_b32 m0, s60
	s_nop 0
	global_load_lds_dwordx4 v185, s[88:89]
	s_waitcnt vmcnt(8)
	s_waitcnt lgkmcnt(0)
	s_barrier
	s_setprio 1
	v_mfma_f32_16x16x32_bf16 v[60:63], v[96:99], v[162:165], v[60:63]
	v_mfma_f32_16x16x32_bf16 v[52:55], v[136:139], v[162:165], v[52:55]
	v_mfma_f32_16x16x32_bf16 v[44:47], v[96:99], v[170:173], v[44:47]
	v_mfma_f32_16x16x32_bf16 v[36:39], v[136:139], v[170:173], v[36:39]
	v_mfma_f32_16x16x32_bf16 v[28:31], v[96:99], v[178:181], v[28:31]
	v_mfma_f32_16x16x32_bf16 v[20:23], v[136:139], v[178:181], v[20:23]
	v_mfma_f32_16x16x32_bf16 v[12:15], v[96:99], v[196:199], v[12:15]
	v_mfma_f32_16x16x32_bf16 v[4:7], v[136:139], v[196:199], v[4:7]
	v_mfma_f32_16x16x32_bf16 v[60:63], v[116:119], v[166:169], v[60:63]
	v_mfma_f32_16x16x32_bf16 v[52:55], v[140:143], v[166:169], v[52:55]
	v_mfma_f32_16x16x32_bf16 v[44:47], v[116:119], v[174:177], v[44:47]
	v_mfma_f32_16x16x32_bf16 v[36:39], v[140:143], v[174:177], v[36:39]
	v_mfma_f32_16x16x32_bf16 v[28:31], v[116:119], v[192:195], v[28:31]
	v_mfma_f32_16x16x32_bf16 v[20:23], v[140:143], v[192:195], v[20:23]
	v_mfma_f32_16x16x32_bf16 v[12:15], v[116:119], v[200:203], v[12:15]
	v_mfma_f32_16x16x32_bf16 v[4:7], v[140:143], v[200:203], v[4:7]
	s_setprio 0
	s_setprio 1
	v_mfma_f32_16x16x32_bf16 v[56:59], v[144:147], v[162:165], v[56:59]
	v_mfma_f32_16x16x32_bf16 v[48:51], v[152:155], v[162:165], v[48:51]
	v_mfma_f32_16x16x32_bf16 v[40:43], v[144:147], v[170:173], v[40:43]
	v_mfma_f32_16x16x32_bf16 v[32:35], v[152:155], v[170:173], v[32:35]
	v_mfma_f32_16x16x32_bf16 v[24:27], v[144:147], v[178:181], v[24:27]
	v_mfma_f32_16x16x32_bf16 v[16:19], v[152:155], v[178:181], v[16:19]
	v_mfma_f32_16x16x32_bf16 v[8:11], v[144:147], v[196:199], v[8:11]
	v_mfma_f32_16x16x32_bf16 v[0:3], v[152:155], v[196:199], v[0:3]
	v_mfma_f32_16x16x32_bf16 v[56:59], v[148:151], v[166:169], v[56:59]
	v_mfma_f32_16x16x32_bf16 v[48:51], v[158:161], v[166:169], v[48:51]
	v_mfma_f32_16x16x32_bf16 v[40:43], v[148:151], v[174:177], v[40:43]
	v_mfma_f32_16x16x32_bf16 v[32:35], v[158:161], v[174:177], v[32:35]
	v_mfma_f32_16x16x32_bf16 v[24:27], v[148:151], v[192:195], v[24:27]
	v_mfma_f32_16x16x32_bf16 v[16:19], v[158:161], v[192:195], v[16:19]
	v_mfma_f32_16x16x32_bf16 v[8:11], v[148:151], v[200:203], v[8:11]
	v_mfma_f32_16x16x32_bf16 v[0:3], v[158:161], v[200:203], v[0:3]
	s_setprio 0
	s_add_i32 s87, 0, 0x18000
	s_add_i32 s88, 0, 0x1c000
	s_barrier
	v_add_u32_e32 v140, s87, v187
	v_add_u32_e32 v158, s88, v187
	ds_read_b128 v[96:99], v140
	ds_read_b128 v[116:119], v140 offset:1024
	ds_read_b128 v[136:139], v140 offset:2048
	ds_read_b128 v[140:143], v140 offset:3072
	ds_read_b128 v[144:147], v158
	ds_read_b128 v[148:151], v158 offset:1024
	ds_read_b128 v[152:155], v158 offset:2048
	ds_read_b128 v[158:161], v158 offset:3072
	s_mov_b32 m0, s61
	ds_read_b128 v[162:165], v191 offset:32768
	ds_read_b128 v[166:169], v191 offset:33792
	ds_read_b128 v[170:173], v191 offset:34816
	ds_read_b128 v[174:177], v191 offset:35840
	ds_read_b128 v[178:181], v191 offset:36864
	ds_read_b128 v[192:195], v191 offset:37888
	ds_read_b128 v[196:199], v191 offset:38912
	ds_read_b128 v[200:203], v191 offset:39936
	s_nop 0
	global_load_lds_dwordx4 v184, s[56:57]
	s_mov_b32 m0, s62
	s_nop 0
	global_load_lds_dwordx4 v185, s[56:57]
	s_waitcnt vmcnt(8)
	s_waitcnt lgkmcnt(0)
	s_barrier
	s_setprio 1
	v_mfma_f32_16x16x32_bf16 v[132:135], v[96:99], v[162:165], v[132:135]
	v_mfma_f32_16x16x32_bf16 v[124:127], v[136:139], v[162:165], v[124:127]
	v_mfma_f32_16x16x32_bf16 v[112:115], v[96:99], v[170:173], v[112:115]
	v_mfma_f32_16x16x32_bf16 v[104:107], v[136:139], v[170:173], v[104:107]
	v_mfma_f32_16x16x32_bf16 v[92:95], v[96:99], v[178:181], v[92:95]
	v_mfma_f32_16x16x32_bf16 v[84:87], v[136:139], v[178:181], v[84:87]
	v_mfma_f32_16x16x32_bf16 v[76:79], v[96:99], v[196:199], v[76:79]
	v_mfma_f32_16x16x32_bf16 v[68:71], v[136:139], v[196:199], v[68:71]
	v_mfma_f32_16x16x32_bf16 v[132:135], v[116:119], v[166:169], v[132:135]
	v_mfma_f32_16x16x32_bf16 v[124:127], v[140:143], v[166:169], v[124:127]
	v_mfma_f32_16x16x32_bf16 v[112:115], v[116:119], v[174:177], v[112:115]
	v_mfma_f32_16x16x32_bf16 v[104:107], v[140:143], v[174:177], v[104:107]
	v_mfma_f32_16x16x32_bf16 v[92:95], v[116:119], v[192:195], v[92:95]
	v_mfma_f32_16x16x32_bf16 v[84:87], v[140:143], v[192:195], v[84:87]
	v_mfma_f32_16x16x32_bf16 v[76:79], v[116:119], v[200:203], v[76:79]
	v_mfma_f32_16x16x32_bf16 v[68:71], v[140:143], v[200:203], v[68:71]
	s_setprio 0
	s_setprio 1
	v_mfma_f32_16x16x32_bf16 v[128:131], v[144:147], v[162:165], v[128:131]
	v_mfma_f32_16x16x32_bf16 v[120:123], v[152:155], v[162:165], v[120:123]
	v_mfma_f32_16x16x32_bf16 v[108:111], v[144:147], v[170:173], v[108:111]
	v_mfma_f32_16x16x32_bf16 v[100:103], v[152:155], v[170:173], v[100:103]
	v_mfma_f32_16x16x32_bf16 v[88:91], v[144:147], v[178:181], v[88:91]
	v_mfma_f32_16x16x32_bf16 v[80:83], v[152:155], v[178:181], v[80:83]
	v_mfma_f32_16x16x32_bf16 v[72:75], v[144:147], v[196:199], v[72:75]
	v_mfma_f32_16x16x32_bf16 v[64:67], v[152:155], v[196:199], v[64:67]
	v_mfma_f32_16x16x32_bf16 v[128:131], v[148:151], v[166:169], v[128:131]
	v_mfma_f32_16x16x32_bf16 v[120:123], v[158:161], v[166:169], v[120:123]
	v_mfma_f32_16x16x32_bf16 v[108:111], v[148:151], v[174:177], v[108:111]
	v_mfma_f32_16x16x32_bf16 v[100:103], v[158:161], v[174:177], v[100:103]
	v_mfma_f32_16x16x32_bf16 v[88:91], v[148:151], v[192:195], v[88:91]
	v_mfma_f32_16x16x32_bf16 v[80:83], v[158:161], v[192:195], v[80:83]
	v_mfma_f32_16x16x32_bf16 v[72:75], v[148:151], v[200:203], v[72:75]
	v_mfma_f32_16x16x32_bf16 v[64:67], v[158:161], v[200:203], v[64:67]
	s_setprio 0
	s_add_u32 s54, s54, 0x80
	s_addc_u32 s55, s55, 0
	s_add_i32 s56, s87, s3
	s_barrier
	s_mov_b32 m0, s56
	ds_read_b128 v[162:165], v191 offset:49152
	ds_read_b128 v[166:169], v191 offset:50176
	ds_read_b128 v[170:173], v191 offset:51200
	ds_read_b128 v[174:177], v191 offset:52224
	ds_read_b128 v[178:181], v191 offset:53248
	ds_read_b128 v[192:195], v191 offset:54272
	ds_read_b128 v[196:199], v191 offset:55296
	ds_read_b128 v[200:203], v191 offset:56320
	s_nop 0
	global_load_lds_dwordx4 v182, s[54:55]
	s_add_i32 m0, s56, 0x2000
	s_nop 0
	global_load_lds_dwordx4 v183, s[54:55]
	s_add_u32 s54, s58, 0x80
	s_addc_u32 s55, s59, 0
	s_add_i32 s56, s88, s3
	s_mov_b32 m0, s56
	s_nop 0
	global_load_lds_dwordx4 v182, s[54:55]
	s_add_i32 m0, s56, 0x2000
	s_add_u32 s52, s52, 0x80
	global_load_lds_dwordx4 v183, s[54:55]
	s_addc_u32 s53, s53, 0
	v_mov_b32_e32 v204, v185
	v_mov_b32_e32 v205, v184
	s_mov_b32 m0, s66
	s_nop 0
	global_load_lds_dwordx4 v205, s[52:53]
	s_mov_b32 m0, s67
	s_nop 0
	global_load_lds_dwordx4 v204, s[52:53]
	s_waitcnt vmcnt(8)
	s_waitcnt lgkmcnt(0)
	s_barrier
	s_setprio 1
	v_mfma_f32_16x16x32_bf16 v[60:63], v[96:99], v[162:165], v[60:63]
	v_mfma_f32_16x16x32_bf16 v[52:55], v[136:139], v[162:165], v[52:55]
	v_mfma_f32_16x16x32_bf16 v[44:47], v[96:99], v[170:173], v[44:47]
	v_mfma_f32_16x16x32_bf16 v[36:39], v[136:139], v[170:173], v[36:39]
	v_mfma_f32_16x16x32_bf16 v[28:31], v[96:99], v[178:181], v[28:31]
	v_mfma_f32_16x16x32_bf16 v[20:23], v[136:139], v[178:181], v[20:23]
	v_mfma_f32_16x16x32_bf16 v[12:15], v[96:99], v[196:199], v[12:15]
	v_mfma_f32_16x16x32_bf16 v[4:7], v[136:139], v[196:199], v[4:7]
	v_mfma_f32_16x16x32_bf16 v[60:63], v[116:119], v[166:169], v[60:63]
	v_mfma_f32_16x16x32_bf16 v[52:55], v[140:143], v[166:169], v[52:55]
	v_mfma_f32_16x16x32_bf16 v[44:47], v[116:119], v[174:177], v[44:47]
	v_mfma_f32_16x16x32_bf16 v[36:39], v[140:143], v[174:177], v[36:39]
	v_mfma_f32_16x16x32_bf16 v[28:31], v[116:119], v[192:195], v[28:31]
	v_mfma_f32_16x16x32_bf16 v[20:23], v[140:143], v[192:195], v[20:23]
	v_mfma_f32_16x16x32_bf16 v[12:15], v[116:119], v[200:203], v[12:15]
	v_mfma_f32_16x16x32_bf16 v[4:7], v[140:143], v[200:203], v[4:7]
	s_setprio 0
	s_setprio 1
	v_mfma_f32_16x16x32_bf16 v[56:59], v[144:147], v[162:165], v[56:59]
	v_mfma_f32_16x16x32_bf16 v[48:51], v[152:155], v[162:165], v[48:51]
	v_mfma_f32_16x16x32_bf16 v[40:43], v[144:147], v[170:173], v[40:43]
	v_mfma_f32_16x16x32_bf16 v[32:35], v[152:155], v[170:173], v[32:35]
	v_mfma_f32_16x16x32_bf16 v[24:27], v[144:147], v[178:181], v[24:27]
	v_mfma_f32_16x16x32_bf16 v[16:19], v[152:155], v[178:181], v[16:19]
	v_mfma_f32_16x16x32_bf16 v[8:11], v[144:147], v[196:199], v[8:11]
	v_mfma_f32_16x16x32_bf16 v[0:3], v[152:155], v[196:199], v[0:3]
	v_mfma_f32_16x16x32_bf16 v[56:59], v[148:151], v[166:169], v[56:59]
	v_mfma_f32_16x16x32_bf16 v[48:51], v[158:161], v[166:169], v[48:51]
	v_mfma_f32_16x16x32_bf16 v[40:43], v[148:151], v[174:177], v[40:43]
	v_mfma_f32_16x16x32_bf16 v[32:35], v[158:161], v[174:177], v[32:35]
	v_mfma_f32_16x16x32_bf16 v[24:27], v[148:151], v[192:195], v[24:27]
	v_mfma_f32_16x16x32_bf16 v[16:19], v[158:161], v[192:195], v[16:19]
	v_mfma_f32_16x16x32_bf16 v[8:11], v[148:151], v[200:203], v[8:11]
	v_mfma_f32_16x16x32_bf16 v[0:3], v[158:161], v[200:203], v[0:3]
	s_setprio 0
	s_add_u32 s78, s78, 0x100
	s_addc_u32 s79, s79, 0
	s_add_u32 s80, s80, 0x100
	s_addc_u32 s81, s81, 0
	s_add_u32 s82, s82, 0x100
	s_addc_u32 s83, s83, 0
	s_add_u32 s84, s84, 0x100
	s_addc_u32 s85, s85, 0
	s_cmp_ge_i32 s86, s2
	s_mov_b32 s52, s86
	s_barrier
	s_cbranch_scc0 .LBB0_1281
	s_and_b64 vcc, exec, s[18:19]
	s_cbranch_vccz .LBB0_1284

.LBB0_1434:
	ds_read_b128 v[68:71], v217
	ds_read_b128 v[80:83], v217 offset:1024
	ds_read_b128 v[92:95], v217 offset:2048
	ds_read_b128 v[104:107], v217 offset:3072
	ds_read_b128 v[116:119], v218
	ds_read_b128 v[128:131], v218 offset:1024
	ds_read_b128 v[136:139], v218 offset:2048
	ds_read_b128 v[140:143], v218 offset:3072
	s_add_i32 s86, s12, 2
	s_add_u32 s52, s84, 0xffffff80
	s_addc_u32 s53, s85, -1
	s_add_i32 m0, s33, 0xc000
	s_add_i32 s87, s33, 0xe000
	s_cmp_eq_u32 s62, s12
	s_cselect_b32 s12, s46, s82
	s_cselect_b32 s13, s47, s83
	s_cselect_b32 s49, s45, s79
	s_cselect_b32 s48, s44, s78
	s_cselect_b32 s51, s41, s85
	s_cselect_b32 s50, s40, s84
	v_mov_b32_e32 v192, v206
	v_mov_b32_e32 v193, v204
	ds_read_b128 v[144:147], v219
	ds_read_b128 v[148:151], v219 offset:1024
	ds_read_b128 v[156:159], v219 offset:2048
	ds_read_b128 v[168:171], v219 offset:3072
	ds_read_b128 v[176:179], v219 offset:4096
	ds_read_b128 v[180:183], v219 offset:5120
	ds_read_b128 v[184:187], v219 offset:6144
	ds_read_b128 v[188:191], v219 offset:7168
	s_nop 0
	global_load_lds_dwordx4 v193, s[52:53] nt
	s_mov_b32 m0, s87
	s_nop 0
	global_load_lds_dwordx4 v192, s[52:53] nt
	s_waitcnt vmcnt(8)
	s_waitcnt lgkmcnt(0)
	s_barrier
	s_setprio 1
	v_mfma_f32_16x16x32_bf16 v[172:175], v[68:71], v[144:147], v[172:175]
	v_mfma_f32_16x16x32_bf16 v[164:167], v[92:95], v[144:147], v[164:167]
	v_mfma_f32_16x16x32_bf16 v[132:135], v[68:71], v[156:159], v[132:135]
	v_mfma_f32_16x16x32_bf16 v[124:127], v[92:95], v[156:159], v[124:127]
	v_mfma_f32_16x16x32_bf16 v[108:111], v[68:71], v[176:179], v[108:111]
	v_mfma_f32_16x16x32_bf16 v[100:103], v[92:95], v[176:179], v[100:103]
	v_mfma_f32_16x16x32_bf16 v[84:87], v[68:71], v[184:187], v[84:87]
	v_mfma_f32_16x16x32_bf16 v[76:79], v[92:95], v[184:187], v[76:79]
	v_mfma_f32_16x16x32_bf16 v[172:175], v[80:83], v[148:151], v[172:175]
	v_mfma_f32_16x16x32_bf16 v[164:167], v[104:107], v[148:151], v[164:167]
	v_mfma_f32_16x16x32_bf16 v[132:135], v[80:83], v[168:171], v[132:135]
	v_mfma_f32_16x16x32_bf16 v[124:127], v[104:107], v[168:171], v[124:127]
	v_mfma_f32_16x16x32_bf16 v[108:111], v[80:83], v[180:183], v[108:111]
	v_mfma_f32_16x16x32_bf16 v[100:103], v[104:107], v[180:183], v[100:103]
	v_mfma_f32_16x16x32_bf16 v[84:87], v[80:83], v[188:191], v[84:87]
	v_mfma_f32_16x16x32_bf16 v[76:79], v[104:107], v[188:191], v[76:79]
	s_setprio 0
	s_setprio 1
	v_mfma_f32_16x16x32_bf16 v[160:163], v[116:119], v[144:147], v[160:163]
	v_mfma_f32_16x16x32_bf16 v[120:123], v[116:119], v[156:159], v[120:123]
	v_mfma_f32_16x16x32_bf16 v[112:115], v[136:139], v[156:159], v[112:115]
	v_mfma_f32_16x16x32_bf16 v[96:99], v[116:119], v[176:179], v[96:99]
	v_mfma_f32_16x16x32_bf16 v[88:91], v[136:139], v[176:179], v[88:91]
	v_mfma_f32_16x16x32_bf16 v[72:75], v[116:119], v[184:187], v[72:75]
	v_mfma_f32_16x16x32_bf16 v[64:67], v[136:139], v[184:187], v[64:67]
	v_mfma_f32_16x16x32_bf16 v[160:163], v[128:131], v[148:151], v[160:163]
	v_mfma_f32_16x16x32_bf16 v[144:147], v[136:139], v[144:147], v[152:155]
	v_mfma_f32_16x16x32_bf16 v[120:123], v[128:131], v[168:171], v[120:123]
	v_mfma_f32_16x16x32_bf16 v[112:115], v[140:143], v[168:171], v[112:115]
	v_mfma_f32_16x16x32_bf16 v[96:99], v[128:131], v[180:183], v[96:99]
	v_mfma_f32_16x16x32_bf16 v[88:91], v[140:143], v[180:183], v[88:91]
	v_mfma_f32_16x16x32_bf16 v[72:75], v[128:131], v[188:191], v[72:75]
	v_mfma_f32_16x16x32_bf16 v[64:67], v[140:143], v[188:191], v[64:67]
	v_mfma_f32_16x16x32_bf16 v[144:147], v[140:143], v[148:151], v[144:147]
	s_setprio 0
	s_cselect_b32 s53, s43, s81
	s_cselect_b32 s52, s42, s80
	s_add_i32 s87, s71, s31
	s_barrier
	v_mov_b32_e32 v192, v214
	s_mov_b64 s[88:89], s[48:49]
	v_mov_b32_e32 v193, v215
	s_mov_b32 m0, s87
	ds_read_b128 v[148:151], v219 offset:16384
	ds_read_b128 v[152:155], v219 offset:17408
	ds_read_b128 v[156:159], v219 offset:18432
	ds_read_b128 v[168:171], v219 offset:19456
	ds_read_b128 v[176:179], v219 offset:20480
	ds_read_b128 v[180:183], v219 offset:21504
	ds_read_b128 v[184:187], v219 offset:22528
	ds_read_b128 v[188:191], v219 offset:23552
	s_nop 0
	global_load_lds_dwordx4 v192, s[88:89] nt
	s_add_i32 m0, s87, 0x2000
	s_add_i32 s87, s72, s31
	global_load_lds_dwordx4 v193, s[88:89] nt
	s_mov_b64 s[88:89], s[52:53]
	v_mov_b32_e32 v192, v214
	v_mov_b32_e32 v193, v215
	s_mov_b32 m0, s87
	s_nop 0
	global_load_lds_dwordx4 v192, s[88:89] nt
	s_add_i32 m0, s87, 0x2000
	v_mov_b32_e32 v192, v206
	global_load_lds_dwordx4 v193, s[88:89] nt
	s_mov_b64 s[88:89], s[12:13]
	v_mov_b32_e32 v193, v204
	s_mov_b32 m0, s33
	s_nop 0
	global_load_lds_dwordx4 v193, s[88:89] nt
	s_mov_b32 m0, s54
	s_nop 0
	global_load_lds_dwordx4 v192, s[88:89] nt
	s_waitcnt vmcnt(8)
	s_waitcnt lgkmcnt(0)
	s_barrier
	s_setprio 1
	v_mfma_f32_16x16x32_bf16 v[60:63], v[68:71], v[148:151], v[60:63]
	v_mfma_f32_16x16x32_bf16 v[56:59], v[92:95], v[148:151], v[56:59]
	v_mfma_f32_16x16x32_bf16 v[44:47], v[68:71], v[156:159], v[44:47]
	v_mfma_f32_16x16x32_bf16 v[40:43], v[92:95], v[156:159], v[40:43]
	v_mfma_f32_16x16x32_bf16 v[28:31], v[68:71], v[176:179], v[28:31]
	v_mfma_f32_16x16x32_bf16 v[24:27], v[92:95], v[176:179], v[24:27]
	v_mfma_f32_16x16x32_bf16 v[12:15], v[68:71], v[184:187], v[12:15]
	v_mfma_f32_16x16x32_bf16 v[8:11], v[92:95], v[184:187], v[8:11]
	v_mfma_f32_16x16x32_bf16 v[60:63], v[80:83], v[152:155], v[60:63]
	v_mfma_f32_16x16x32_bf16 v[56:59], v[104:107], v[152:155], v[56:59]
	v_mfma_f32_16x16x32_bf16 v[44:47], v[80:83], v[168:171], v[44:47]
	v_mfma_f32_16x16x32_bf16 v[40:43], v[104:107], v[168:171], v[40:43]
	v_mfma_f32_16x16x32_bf16 v[28:31], v[80:83], v[180:183], v[28:31]
	v_mfma_f32_16x16x32_bf16 v[24:27], v[104:107], v[180:183], v[24:27]
	v_mfma_f32_16x16x32_bf16 v[12:15], v[80:83], v[188:191], v[12:15]
	v_mfma_f32_16x16x32_bf16 v[8:11], v[104:107], v[188:191], v[8:11]
	s_setprio 0
	s_setprio 1
	v_mfma_f32_16x16x32_bf16 v[52:55], v[116:119], v[148:151], v[52:55]
	v_mfma_f32_16x16x32_bf16 v[48:51], v[136:139], v[148:151], v[48:51]
	v_mfma_f32_16x16x32_bf16 v[36:39], v[116:119], v[156:159], v[36:39]
	v_mfma_f32_16x16x32_bf16 v[32:35], v[136:139], v[156:159], v[32:35]
	v_mfma_f32_16x16x32_bf16 v[20:23], v[116:119], v[176:179], v[20:23]
	v_mfma_f32_16x16x32_bf16 v[16:19], v[136:139], v[176:179], v[16:19]
	v_mfma_f32_16x16x32_bf16 v[4:7], v[116:119], v[184:187], v[4:7]
	v_mfma_f32_16x16x32_bf16 v[0:3], v[136:139], v[184:187], v[0:3]
	v_mfma_f32_16x16x32_bf16 v[52:55], v[128:131], v[152:155], v[52:55]
	v_mfma_f32_16x16x32_bf16 v[48:51], v[140:143], v[152:155], v[48:51]
	v_mfma_f32_16x16x32_bf16 v[36:39], v[128:131], v[168:171], v[36:39]
	v_mfma_f32_16x16x32_bf16 v[32:35], v[140:143], v[168:171], v[32:35]
	v_mfma_f32_16x16x32_bf16 v[20:23], v[128:131], v[180:183], v[20:23]
	v_mfma_f32_16x16x32_bf16 v[16:19], v[140:143], v[180:183], v[16:19]
	v_mfma_f32_16x16x32_bf16 v[4:7], v[128:131], v[188:191], v[4:7]
	v_mfma_f32_16x16x32_bf16 v[0:3], v[140:143], v[188:191], v[0:3]
	s_setprio 0
	s_add_i32 s87, 0, 0x18000
	s_add_i32 s88, 0, 0x1c000
	s_barrier
	v_add_u32_e32 v104, s87, v207
	v_add_u32_e32 v140, s88, v207
	ds_read_b128 v[68:71], v104
	ds_read_b128 v[80:83], v104 offset:1024
	ds_read_b128 v[92:95], v104 offset:2048
	ds_read_b128 v[104:107], v104 offset:3072
	ds_read_b128 v[116:119], v140
	ds_read_b128 v[128:131], v140 offset:1024
	ds_read_b128 v[136:139], v140 offset:2048
	ds_read_b128 v[140:143], v140 offset:3072
	v_mov_b32_e32 v192, v206
	v_mov_b32_e32 v193, v204
	s_mov_b32 m0, s55
	ds_read_b128 v[148:151], v219 offset:32768
	ds_read_b128 v[152:155], v219 offset:33792
	ds_read_b128 v[156:159], v219 offset:34816
	ds_read_b128 v[168:171], v219 offset:35840
	ds_read_b128 v[176:179], v219 offset:36864
	ds_read_b128 v[180:183], v219 offset:37888
	ds_read_b128 v[184:187], v219 offset:38912
	ds_read_b128 v[188:191], v219 offset:39936
	s_nop 0
	global_load_lds_dwordx4 v193, s[50:51] nt
	s_mov_b32 m0, s56
	s_nop 0
	global_load_lds_dwordx4 v192, s[50:51] nt
	s_waitcnt vmcnt(8)
	s_waitcnt lgkmcnt(0)
	s_barrier
	s_setprio 1
	v_mfma_f32_16x16x32_bf16 v[172:175], v[68:71], v[148:151], v[172:175]
	v_mfma_f32_16x16x32_bf16 v[164:167], v[92:95], v[148:151], v[164:167]
	v_mfma_f32_16x16x32_bf16 v[132:135], v[68:71], v[156:159], v[132:135]
	v_mfma_f32_16x16x32_bf16 v[124:127], v[92:95], v[156:159], v[124:127]
	v_mfma_f32_16x16x32_bf16 v[108:111], v[68:71], v[176:179], v[108:111]
	v_mfma_f32_16x16x32_bf16 v[100:103], v[92:95], v[176:179], v[100:103]
	v_mfma_f32_16x16x32_bf16 v[84:87], v[68:71], v[184:187], v[84:87]
	v_mfma_f32_16x16x32_bf16 v[76:79], v[92:95], v[184:187], v[76:79]
	v_mfma_f32_16x16x32_bf16 v[172:175], v[80:83], v[152:155], v[172:175]
	v_mfma_f32_16x16x32_bf16 v[164:167], v[104:107], v[152:155], v[164:167]
	v_mfma_f32_16x16x32_bf16 v[132:135], v[80:83], v[168:171], v[132:135]
	v_mfma_f32_16x16x32_bf16 v[124:127], v[104:107], v[168:171], v[124:127]
	v_mfma_f32_16x16x32_bf16 v[108:111], v[80:83], v[180:183], v[108:111]
	v_mfma_f32_16x16x32_bf16 v[100:103], v[104:107], v[180:183], v[100:103]
	v_mfma_f32_16x16x32_bf16 v[84:87], v[80:83], v[188:191], v[84:87]
	v_mfma_f32_16x16x32_bf16 v[76:79], v[104:107], v[188:191], v[76:79]
	s_setprio 0
	s_setprio 1
	v_mfma_f32_16x16x32_bf16 v[160:163], v[116:119], v[148:151], v[160:163]
	v_mfma_f32_16x16x32_bf16 v[144:147], v[136:139], v[148:151], v[144:147]
	v_mfma_f32_16x16x32_bf16 v[120:123], v[116:119], v[156:159], v[120:123]
	v_mfma_f32_16x16x32_bf16 v[112:115], v[136:139], v[156:159], v[112:115]
	v_mfma_f32_16x16x32_bf16 v[96:99], v[116:119], v[176:179], v[96:99]
	v_mfma_f32_16x16x32_bf16 v[88:91], v[136:139], v[176:179], v[88:91]
	v_mfma_f32_16x16x32_bf16 v[72:75], v[116:119], v[184:187], v[72:75]
	v_mfma_f32_16x16x32_bf16 v[64:67], v[136:139], v[184:187], v[64:67]
	v_mfma_f32_16x16x32_bf16 v[160:163], v[128:131], v[152:155], v[160:163]
	v_mfma_f32_16x16x32_bf16 v[152:155], v[140:143], v[152:155], v[144:147]
	v_mfma_f32_16x16x32_bf16 v[120:123], v[128:131], v[168:171], v[120:123]
	v_mfma_f32_16x16x32_bf16 v[112:115], v[140:143], v[168:171], v[112:115]
	v_mfma_f32_16x16x32_bf16 v[96:99], v[128:131], v[180:183], v[96:99]
	v_mfma_f32_16x16x32_bf16 v[88:91], v[140:143], v[180:183], v[88:91]
	v_mfma_f32_16x16x32_bf16 v[72:75], v[128:131], v[188:191], v[72:75]
	v_mfma_f32_16x16x32_bf16 v[64:67], v[140:143], v[188:191], v[64:67]
	s_setprio 0
	s_add_u32 s48, s48, 0x80
	s_addc_u32 s49, s49, 0
	s_add_i32 s50, s87, s31
	s_barrier
	v_mov_b32_e32 v192, v214
	v_mov_b32_e32 v193, v215
	s_mov_b32 m0, s50
	ds_read_b128 v[144:147], v219 offset:49152
	ds_read_b128 v[148:151], v219 offset:50176
	ds_read_b128 v[156:159], v219 offset:51200
	ds_read_b128 v[168:171], v219 offset:52224
	ds_read_b128 v[176:179], v219 offset:53248
	ds_read_b128 v[180:183], v219 offset:54272
	ds_read_b128 v[184:187], v219 offset:55296
	ds_read_b128 v[188:191], v219 offset:56320
	s_nop 0
	global_load_lds_dwordx4 v192, s[48:49] nt
	s_add_i32 m0, s50, 0x2000
	v_mov_b32_e32 v192, v214
	global_load_lds_dwordx4 v193, s[48:49] nt
	s_add_u32 s48, s52, 0x80
	s_addc_u32 s49, s53, 0
	s_add_i32 s50, s88, s31
	v_mov_b32_e32 v193, v215
	s_mov_b32 m0, s50
	s_nop 0
	global_load_lds_dwordx4 v192, s[48:49] nt
	s_add_i32 m0, s50, 0x2000
	s_add_u32 s12, s12, 0x80
	global_load_lds_dwordx4 v193, s[48:49] nt
	s_addc_u32 s13, s13, 0
	v_mov_b32_e32 v192, v206
	v_mov_b32_e32 v193, v204
	s_mov_b32 m0, s60
	s_nop 0
	global_load_lds_dwordx4 v193, s[12:13] nt
	s_mov_b32 m0, s61
	s_nop 0
	global_load_lds_dwordx4 v192, s[12:13] nt
	s_waitcnt vmcnt(8)
	s_waitcnt lgkmcnt(0)
	s_barrier
	s_setprio 1
	v_mfma_f32_16x16x32_bf16 v[60:63], v[68:71], v[144:147], v[60:63]
	v_mfma_f32_16x16x32_bf16 v[56:59], v[92:95], v[144:147], v[56:59]
	v_mfma_f32_16x16x32_bf16 v[44:47], v[68:71], v[156:159], v[44:47]
	v_mfma_f32_16x16x32_bf16 v[40:43], v[92:95], v[156:159], v[40:43]
	v_mfma_f32_16x16x32_bf16 v[28:31], v[68:71], v[176:179], v[28:31]
	v_mfma_f32_16x16x32_bf16 v[24:27], v[92:95], v[176:179], v[24:27]
	v_mfma_f32_16x16x32_bf16 v[12:15], v[68:71], v[184:187], v[12:15]
	v_mfma_f32_16x16x32_bf16 v[8:11], v[92:95], v[184:187], v[8:11]
	v_mfma_f32_16x16x32_bf16 v[60:63], v[80:83], v[148:151], v[60:63]
	v_mfma_f32_16x16x32_bf16 v[56:59], v[104:107], v[148:151], v[56:59]
	v_mfma_f32_16x16x32_bf16 v[44:47], v[80:83], v[168:171], v[44:47]
	v_mfma_f32_16x16x32_bf16 v[40:43], v[104:107], v[168:171], v[40:43]
	v_mfma_f32_16x16x32_bf16 v[28:31], v[80:83], v[180:183], v[28:31]
	v_mfma_f32_16x16x32_bf16 v[24:27], v[104:107], v[180:183], v[24:27]
	v_mfma_f32_16x16x32_bf16 v[12:15], v[80:83], v[188:191], v[12:15]
	v_mfma_f32_16x16x32_bf16 v[8:11], v[104:107], v[188:191], v[8:11]
	s_setprio 0
	s_setprio 1
	v_mfma_f32_16x16x32_bf16 v[52:55], v[116:119], v[144:147], v[52:55]
	v_mfma_f32_16x16x32_bf16 v[48:51], v[136:139], v[144:147], v[48:51]
	v_mfma_f32_16x16x32_bf16 v[36:39], v[116:119], v[156:159], v[36:39]
	v_mfma_f32_16x16x32_bf16 v[32:35], v[136:139], v[156:159], v[32:35]
	v_mfma_f32_16x16x32_bf16 v[20:23], v[116:119], v[176:179], v[20:23]
	v_mfma_f32_16x16x32_bf16 v[16:19], v[136:139], v[176:179], v[16:19]
	v_mfma_f32_16x16x32_bf16 v[4:7], v[116:119], v[184:187], v[4:7]
	v_mfma_f32_16x16x32_bf16 v[0:3], v[136:139], v[184:187], v[0:3]
	v_mfma_f32_16x16x32_bf16 v[52:55], v[128:131], v[148:151], v[52:55]
	v_mfma_f32_16x16x32_bf16 v[48:51], v[140:143], v[148:151], v[48:51]
	v_mfma_f32_16x16x32_bf16 v[36:39], v[128:131], v[168:171], v[36:39]
	v_mfma_f32_16x16x32_bf16 v[32:35], v[140:143], v[168:171], v[32:35]
	v_mfma_f32_16x16x32_bf16 v[20:23], v[128:131], v[180:183], v[20:23]
	v_mfma_f32_16x16x32_bf16 v[16:19], v[140:143], v[180:183], v[16:19]
	v_mfma_f32_16x16x32_bf16 v[4:7], v[128:131], v[188:191], v[4:7]
	v_mfma_f32_16x16x32_bf16 v[0:3], v[140:143], v[188:191], v[0:3]
	s_setprio 0
	s_add_u32 s78, s78, 0x100
	s_addc_u32 s79, s79, 0
	s_add_u32 s80, s80, 0x100
	s_addc_u32 s81, s81, 0
	s_add_u32 s82, s82, 0x100
	s_addc_u32 s83, s83, 0
	s_add_u32 s84, s84, 0x100
	s_addc_u32 s85, s85, 0
	s_cmp_ge_i32 s86, s3
	s_mov_b32 s12, s86
	s_barrier
	s_cbranch_scc0 .LBB0_1434
	s_and_b64 vcc, exec, s[28:29]
	s_cbranch_vccz .LBB0_1437

.LBB0_1671:
	ds_read_b128 v[128:131], v217
	ds_read_b128 v[132:135], v217 offset:1024
	ds_read_b128 v[136:139], v217 offset:2048
	ds_read_b128 v[140:143], v217 offset:3072
	ds_read_b128 v[144:147], v218
	ds_read_b128 v[148:151], v218 offset:1024
	ds_read_b128 v[152:155], v218 offset:2048
	ds_read_b128 v[156:159], v218 offset:3072
	s_add_i32 s78, s44, 2
	s_add_u32 s50, s76, 0xffffff80
	s_addc_u32 s51, s77, -1
	s_add_i32 m0, s53, 0xc000
	s_add_i32 s79, s53, 0xe000
	s_cmp_eq_u32 s62, s44
	s_cselect_b32 s44, s42, s74
	s_cselect_b32 s45, s43, s75
	s_cselect_b32 s47, s41, s71
	s_cselect_b32 s46, s40, s70
	s_cselect_b32 s49, s37, s77
	s_cselect_b32 s48, s36, s76
	ds_read_b128 v[160:163], v219
	ds_read_b128 v[164:167], v219 offset:1024
	ds_read_b128 v[168:171], v219 offset:2048
	ds_read_b128 v[172:175], v219 offset:3072
	ds_read_b128 v[176:179], v219 offset:4096
	ds_read_b128 v[180:183], v219 offset:5120
	ds_read_b128 v[184:187], v219 offset:6144
	ds_read_b128 v[188:191], v219 offset:7168
	s_nop 0
	global_load_lds_dwordx4 v212, s[50:51]
	s_mov_b32 m0, s79
	s_nop 0
	global_load_lds_dwordx4 v213, s[50:51]
	s_waitcnt vmcnt(8)
	s_waitcnt lgkmcnt(0)
	s_barrier
	s_setprio 1
	v_mfma_f32_16x16x32_bf16 v[116:119], v[128:131], v[160:163], v[116:119]
	v_mfma_f32_16x16x32_bf16 v[124:127], v[136:139], v[160:163], v[124:127]
	v_mfma_f32_16x16x32_bf16 v[108:111], v[128:131], v[168:171], v[108:111]
	v_mfma_f32_16x16x32_bf16 v[104:107], v[136:139], v[168:171], v[104:107]
	v_mfma_f32_16x16x32_bf16 v[92:95], v[128:131], v[176:179], v[92:95]
	v_mfma_f32_16x16x32_bf16 v[88:91], v[136:139], v[176:179], v[88:91]
	v_mfma_f32_16x16x32_bf16 v[76:79], v[128:131], v[184:187], v[76:79]
	v_mfma_f32_16x16x32_bf16 v[72:75], v[136:139], v[184:187], v[72:75]
	v_mfma_f32_16x16x32_bf16 v[116:119], v[132:135], v[164:167], v[116:119]
	v_mfma_f32_16x16x32_bf16 v[124:127], v[140:143], v[164:167], v[124:127]
	v_mfma_f32_16x16x32_bf16 v[108:111], v[132:135], v[172:175], v[108:111]
	v_mfma_f32_16x16x32_bf16 v[104:107], v[140:143], v[172:175], v[104:107]
	v_mfma_f32_16x16x32_bf16 v[92:95], v[132:135], v[180:183], v[92:95]
	v_mfma_f32_16x16x32_bf16 v[88:91], v[140:143], v[180:183], v[88:91]
	v_mfma_f32_16x16x32_bf16 v[76:79], v[132:135], v[188:191], v[76:79]
	v_mfma_f32_16x16x32_bf16 v[72:75], v[140:143], v[188:191], v[72:75]
	s_setprio 0
	s_setprio 1
	v_mfma_f32_16x16x32_bf16 v[120:123], v[144:147], v[160:163], v[120:123]
	v_mfma_f32_16x16x32_bf16 v[112:115], v[152:155], v[160:163], v[112:115]
	v_mfma_f32_16x16x32_bf16 v[100:103], v[144:147], v[168:171], v[100:103]
	v_mfma_f32_16x16x32_bf16 v[96:99], v[152:155], v[168:171], v[96:99]
	v_mfma_f32_16x16x32_bf16 v[84:87], v[144:147], v[176:179], v[84:87]
	v_mfma_f32_16x16x32_bf16 v[80:83], v[152:155], v[176:179], v[80:83]
	v_mfma_f32_16x16x32_bf16 v[68:71], v[144:147], v[184:187], v[68:71]
	v_mfma_f32_16x16x32_bf16 v[64:67], v[152:155], v[184:187], v[64:67]
	v_mfma_f32_16x16x32_bf16 v[120:123], v[148:151], v[164:167], v[120:123]
	v_mfma_f32_16x16x32_bf16 v[112:115], v[156:159], v[164:167], v[112:115]
	v_mfma_f32_16x16x32_bf16 v[100:103], v[148:151], v[172:175], v[100:103]
	v_mfma_f32_16x16x32_bf16 v[96:99], v[156:159], v[172:175], v[96:99]
	v_mfma_f32_16x16x32_bf16 v[84:87], v[148:151], v[180:183], v[84:87]
	v_mfma_f32_16x16x32_bf16 v[80:83], v[156:159], v[180:183], v[80:83]
	v_mfma_f32_16x16x32_bf16 v[68:71], v[148:151], v[188:191], v[68:71]
	v_mfma_f32_16x16x32_bf16 v[64:67], v[156:159], v[188:191], v[64:67]
	s_setprio 0
	s_cselect_b32 s51, s39, s73
	s_cselect_b32 s50, s38, s72
	s_add_i32 s79, s63, s52
	s_barrier
	s_mov_b64 s[80:81], s[46:47]
	s_mov_b32 m0, s79
	ds_read_b128 v[160:163], v219 offset:16384
	ds_read_b128 v[164:167], v219 offset:17408
	ds_read_b128 v[168:171], v219 offset:18432
	ds_read_b128 v[172:175], v219 offset:19456
	ds_read_b128 v[176:179], v219 offset:20480
	ds_read_b128 v[180:183], v219 offset:21504
	ds_read_b128 v[184:187], v219 offset:22528
	ds_read_b128 v[188:191], v219 offset:23552
	s_nop 0
	global_load_lds_dwordx4 v212, s[80:81]
	s_add_i32 m0, s79, 0x2000
	s_add_i32 s79, s64, s52
	global_load_lds_dwordx4 v213, s[80:81]
	s_mov_b64 s[80:81], s[50:51]
	s_mov_b32 m0, s79
	s_nop 0
	global_load_lds_dwordx4 v212, s[80:81]
	s_add_i32 m0, s79, 0x2000
	s_nop 0
	global_load_lds_dwordx4 v213, s[80:81]
	s_mov_b64 s[80:81], s[44:45]
	s_mov_b32 m0, s53
	s_nop 0
	global_load_lds_dwordx4 v212, s[80:81]
	s_mov_b32 m0, s54
	s_nop 0
	global_load_lds_dwordx4 v213, s[80:81]
	s_waitcnt vmcnt(8)
	s_waitcnt lgkmcnt(0)
	s_barrier
	s_setprio 1
	v_mfma_f32_16x16x32_bf16 v[60:63], v[128:131], v[160:163], v[60:63]
	v_mfma_f32_16x16x32_bf16 v[56:59], v[136:139], v[160:163], v[56:59]
	v_mfma_f32_16x16x32_bf16 v[44:47], v[128:131], v[168:171], v[44:47]
	v_mfma_f32_16x16x32_bf16 v[40:43], v[136:139], v[168:171], v[40:43]
	v_mfma_f32_16x16x32_bf16 v[28:31], v[128:131], v[176:179], v[28:31]
	v_mfma_f32_16x16x32_bf16 v[24:27], v[136:139], v[176:179], v[24:27]
	v_mfma_f32_16x16x32_bf16 v[12:15], v[128:131], v[184:187], v[12:15]
	v_mfma_f32_16x16x32_bf16 v[8:11], v[136:139], v[184:187], v[8:11]
	v_mfma_f32_16x16x32_bf16 v[60:63], v[132:135], v[164:167], v[60:63]
	v_mfma_f32_16x16x32_bf16 v[56:59], v[140:143], v[164:167], v[56:59]
	v_mfma_f32_16x16x32_bf16 v[44:47], v[132:135], v[172:175], v[44:47]
	v_mfma_f32_16x16x32_bf16 v[40:43], v[140:143], v[172:175], v[40:43]
	v_mfma_f32_16x16x32_bf16 v[28:31], v[132:135], v[180:183], v[28:31]
	v_mfma_f32_16x16x32_bf16 v[24:27], v[140:143], v[180:183], v[24:27]
	v_mfma_f32_16x16x32_bf16 v[12:15], v[132:135], v[188:191], v[12:15]
	v_mfma_f32_16x16x32_bf16 v[8:11], v[140:143], v[188:191], v[8:11]
	s_setprio 0
	s_setprio 1
	v_mfma_f32_16x16x32_bf16 v[52:55], v[144:147], v[160:163], v[52:55]
	v_mfma_f32_16x16x32_bf16 v[48:51], v[152:155], v[160:163], v[48:51]
	v_mfma_f32_16x16x32_bf16 v[36:39], v[144:147], v[168:171], v[36:39]
	v_mfma_f32_16x16x32_bf16 v[32:35], v[152:155], v[168:171], v[32:35]
	v_mfma_f32_16x16x32_bf16 v[20:23], v[144:147], v[176:179], v[20:23]
	v_mfma_f32_16x16x32_bf16 v[16:19], v[152:155], v[176:179], v[16:19]
	v_mfma_f32_16x16x32_bf16 v[4:7], v[144:147], v[184:187], v[4:7]
	v_mfma_f32_16x16x32_bf16 v[0:3], v[152:155], v[184:187], v[0:3]
	v_mfma_f32_16x16x32_bf16 v[52:55], v[148:151], v[164:167], v[52:55]
	v_mfma_f32_16x16x32_bf16 v[48:51], v[156:159], v[164:167], v[48:51]
	v_mfma_f32_16x16x32_bf16 v[36:39], v[148:151], v[172:175], v[36:39]
	v_mfma_f32_16x16x32_bf16 v[32:35], v[156:159], v[172:175], v[32:35]
	v_mfma_f32_16x16x32_bf16 v[20:23], v[148:151], v[180:183], v[20:23]
	v_mfma_f32_16x16x32_bf16 v[16:19], v[156:159], v[180:183], v[16:19]
	v_mfma_f32_16x16x32_bf16 v[4:7], v[148:151], v[188:191], v[4:7]
	v_mfma_f32_16x16x32_bf16 v[0:3], v[156:159], v[188:191], v[0:3]
	s_setprio 0
	s_add_i32 s79, 0, 0x18000
	s_add_i32 s80, 0, 0x1c000
	s_barrier
	v_add_u32_e32 v140, s79, v215
	v_add_u32_e32 v156, s80, v215
	ds_read_b128 v[128:131], v140
	ds_read_b128 v[132:135], v140 offset:1024
	ds_read_b128 v[136:139], v140 offset:2048
	ds_read_b128 v[140:143], v140 offset:3072
	ds_read_b128 v[144:147], v156
	ds_read_b128 v[148:151], v156 offset:1024
	ds_read_b128 v[152:155], v156 offset:2048
	ds_read_b128 v[156:159], v156 offset:3072
	s_mov_b32 m0, s55
	ds_read_b128 v[160:163], v219 offset:32768
	ds_read_b128 v[164:167], v219 offset:33792
	ds_read_b128 v[168:171], v219 offset:34816
	ds_read_b128 v[172:175], v219 offset:35840
	ds_read_b128 v[176:179], v219 offset:36864
	ds_read_b128 v[180:183], v219 offset:37888
	ds_read_b128 v[184:187], v219 offset:38912
	ds_read_b128 v[188:191], v219 offset:39936
	s_nop 0
	global_load_lds_dwordx4 v212, s[48:49]
	s_mov_b32 m0, s56
	s_nop 0
	global_load_lds_dwordx4 v213, s[48:49]
	s_waitcnt vmcnt(8)
	s_waitcnt lgkmcnt(0)
	s_barrier
	s_setprio 1
	v_mfma_f32_16x16x32_bf16 v[116:119], v[128:131], v[160:163], v[116:119]
	v_mfma_f32_16x16x32_bf16 v[124:127], v[136:139], v[160:163], v[124:127]
	v_mfma_f32_16x16x32_bf16 v[108:111], v[128:131], v[168:171], v[108:111]
	v_mfma_f32_16x16x32_bf16 v[104:107], v[136:139], v[168:171], v[104:107]
	v_mfma_f32_16x16x32_bf16 v[92:95], v[128:131], v[176:179], v[92:95]
	v_mfma_f32_16x16x32_bf16 v[88:91], v[136:139], v[176:179], v[88:91]
	v_mfma_f32_16x16x32_bf16 v[76:79], v[128:131], v[184:187], v[76:79]
	v_mfma_f32_16x16x32_bf16 v[72:75], v[136:139], v[184:187], v[72:75]
	v_mfma_f32_16x16x32_bf16 v[116:119], v[132:135], v[164:167], v[116:119]
	v_mfma_f32_16x16x32_bf16 v[124:127], v[140:143], v[164:167], v[124:127]
	v_mfma_f32_16x16x32_bf16 v[108:111], v[132:135], v[172:175], v[108:111]
	v_mfma_f32_16x16x32_bf16 v[104:107], v[140:143], v[172:175], v[104:107]
	v_mfma_f32_16x16x32_bf16 v[92:95], v[132:135], v[180:183], v[92:95]
	v_mfma_f32_16x16x32_bf16 v[88:91], v[140:143], v[180:183], v[88:91]
	v_mfma_f32_16x16x32_bf16 v[76:79], v[132:135], v[188:191], v[76:79]
	v_mfma_f32_16x16x32_bf16 v[72:75], v[140:143], v[188:191], v[72:75]
	s_setprio 0
	s_setprio 1
	v_mfma_f32_16x16x32_bf16 v[120:123], v[144:147], v[160:163], v[120:123]
	v_mfma_f32_16x16x32_bf16 v[112:115], v[152:155], v[160:163], v[112:115]
	v_mfma_f32_16x16x32_bf16 v[100:103], v[144:147], v[168:171], v[100:103]
	v_mfma_f32_16x16x32_bf16 v[96:99], v[152:155], v[168:171], v[96:99]
	v_mfma_f32_16x16x32_bf16 v[84:87], v[144:147], v[176:179], v[84:87]
	v_mfma_f32_16x16x32_bf16 v[80:83], v[152:155], v[176:179], v[80:83]
	v_mfma_f32_16x16x32_bf16 v[68:71], v[144:147], v[184:187], v[68:71]
	v_mfma_f32_16x16x32_bf16 v[64:67], v[152:155], v[184:187], v[64:67]
	v_mfma_f32_16x16x32_bf16 v[120:123], v[148:151], v[164:167], v[120:123]
	v_mfma_f32_16x16x32_bf16 v[112:115], v[156:159], v[164:167], v[112:115]
	v_mfma_f32_16x16x32_bf16 v[100:103], v[148:151], v[172:175], v[100:103]
	v_mfma_f32_16x16x32_bf16 v[96:99], v[156:159], v[172:175], v[96:99]
	v_mfma_f32_16x16x32_bf16 v[84:87], v[148:151], v[180:183], v[84:87]
	v_mfma_f32_16x16x32_bf16 v[80:83], v[156:159], v[180:183], v[80:83]
	v_mfma_f32_16x16x32_bf16 v[68:71], v[148:151], v[188:191], v[68:71]
	v_mfma_f32_16x16x32_bf16 v[64:67], v[156:159], v[188:191], v[64:67]
	s_setprio 0
	s_add_u32 s46, s46, 0x80
	s_addc_u32 s47, s47, 0
	s_add_i32 s48, s79, s52
	s_barrier
	s_mov_b32 m0, s48
	ds_read_b128 v[160:163], v219 offset:49152
	ds_read_b128 v[164:167], v219 offset:50176
	ds_read_b128 v[168:171], v219 offset:51200
	ds_read_b128 v[172:175], v219 offset:52224
	ds_read_b128 v[176:179], v219 offset:53248
	ds_read_b128 v[180:183], v219 offset:54272
	ds_read_b128 v[184:187], v219 offset:55296
	ds_read_b128 v[188:191], v219 offset:56320
	s_nop 0
	global_load_lds_dwordx4 v212, s[46:47]
	s_add_i32 m0, s48, 0x2000
	s_nop 0
	global_load_lds_dwordx4 v213, s[46:47]
	s_add_u32 s46, s50, 0x80
	s_addc_u32 s47, s51, 0
	s_add_i32 s48, s80, s52
	s_mov_b32 m0, s48
	s_nop 0
	global_load_lds_dwordx4 v212, s[46:47]
	s_add_i32 m0, s48, 0x2000
	s_add_u32 s44, s44, 0x80
	global_load_lds_dwordx4 v213, s[46:47]
	s_addc_u32 s45, s45, 0
	v_mov_b32_e32 v194, v213
	v_mov_b32_e32 v195, v212
	s_mov_b32 m0, s60
	s_nop 0
	global_load_lds_dwordx4 v195, s[44:45]
	s_mov_b32 m0, s61
	s_nop 0
	global_load_lds_dwordx4 v194, s[44:45]
	s_waitcnt vmcnt(8)
	s_waitcnt lgkmcnt(0)
	s_barrier
	s_setprio 1
	v_mfma_f32_16x16x32_bf16 v[60:63], v[128:131], v[160:163], v[60:63]
	v_mfma_f32_16x16x32_bf16 v[56:59], v[136:139], v[160:163], v[56:59]
	v_mfma_f32_16x16x32_bf16 v[44:47], v[128:131], v[168:171], v[44:47]
	v_mfma_f32_16x16x32_bf16 v[40:43], v[136:139], v[168:171], v[40:43]
	v_mfma_f32_16x16x32_bf16 v[28:31], v[128:131], v[176:179], v[28:31]
	v_mfma_f32_16x16x32_bf16 v[24:27], v[136:139], v[176:179], v[24:27]
	v_mfma_f32_16x16x32_bf16 v[12:15], v[128:131], v[184:187], v[12:15]
	v_mfma_f32_16x16x32_bf16 v[8:11], v[136:139], v[184:187], v[8:11]
	v_mfma_f32_16x16x32_bf16 v[60:63], v[132:135], v[164:167], v[60:63]
	v_mfma_f32_16x16x32_bf16 v[56:59], v[140:143], v[164:167], v[56:59]
	v_mfma_f32_16x16x32_bf16 v[44:47], v[132:135], v[172:175], v[44:47]
	v_mfma_f32_16x16x32_bf16 v[40:43], v[140:143], v[172:175], v[40:43]
	v_mfma_f32_16x16x32_bf16 v[28:31], v[132:135], v[180:183], v[28:31]
	v_mfma_f32_16x16x32_bf16 v[24:27], v[140:143], v[180:183], v[24:27]
	v_mfma_f32_16x16x32_bf16 v[12:15], v[132:135], v[188:191], v[12:15]
	v_mfma_f32_16x16x32_bf16 v[8:11], v[140:143], v[188:191], v[8:11]
	s_setprio 0
	s_setprio 1
	v_mfma_f32_16x16x32_bf16 v[52:55], v[144:147], v[160:163], v[52:55]
	v_mfma_f32_16x16x32_bf16 v[48:51], v[152:155], v[160:163], v[48:51]
	v_mfma_f32_16x16x32_bf16 v[36:39], v[144:147], v[168:171], v[36:39]
	v_mfma_f32_16x16x32_bf16 v[32:35], v[152:155], v[168:171], v[32:35]
	v_mfma_f32_16x16x32_bf16 v[20:23], v[144:147], v[176:179], v[20:23]
	v_mfma_f32_16x16x32_bf16 v[16:19], v[152:155], v[176:179], v[16:19]
	v_mfma_f32_16x16x32_bf16 v[4:7], v[144:147], v[184:187], v[4:7]
	v_mfma_f32_16x16x32_bf16 v[0:3], v[152:155], v[184:187], v[0:3]
	v_mfma_f32_16x16x32_bf16 v[52:55], v[148:151], v[164:167], v[52:55]
	v_mfma_f32_16x16x32_bf16 v[48:51], v[156:159], v[164:167], v[48:51]
	v_mfma_f32_16x16x32_bf16 v[36:39], v[148:151], v[172:175], v[36:39]
	v_mfma_f32_16x16x32_bf16 v[32:35], v[156:159], v[172:175], v[32:35]
	v_mfma_f32_16x16x32_bf16 v[20:23], v[148:151], v[180:183], v[20:23]
	v_mfma_f32_16x16x32_bf16 v[16:19], v[156:159], v[180:183], v[16:19]
	v_mfma_f32_16x16x32_bf16 v[4:7], v[148:151], v[188:191], v[4:7]
	v_mfma_f32_16x16x32_bf16 v[0:3], v[156:159], v[188:191], v[0:3]
	s_setprio 0
	s_add_u32 s70, s70, 0x100
	s_addc_u32 s71, s71, 0
	s_add_u32 s72, s72, 0x100
	s_addc_u32 s73, s73, 0
	s_add_u32 s74, s74, 0x100
	s_addc_u32 s75, s75, 0
	s_add_u32 s76, s76, 0x100
	s_addc_u32 s77, s77, 0
	s_cmp_ge_i32 s78, s33
	s_mov_b32 s44, s78
	s_barrier
	s_cbranch_scc0 .LBB0_1671
	s_and_b64 vcc, exec, s[20:21]
	s_cbranch_vccz .LBB0_1674

.LBB0_2278:
	s_add_i32 s84, s84, 2
	s_and_b64 s[50:51], s[50:51], exec
	s_cselect_b32 s55, s39, s79
	s_cselect_b32 s54, s38, s47
	s_mov_b32 m0, s62
	s_mov_b64 s[86:87], s[54:55]
	s_cselect_b32 s53, s37, s81
	s_cselect_b32 s52, s36, s80
	ds_read_b128 v[188:191], v184 offset:16384
	ds_read_b128 v[192:195], v184 offset:17408
	ds_read_b128 v[196:199], v184 offset:18432
	ds_read_b128 v[200:203], v184 offset:19456
	ds_read_b128 v[204:207], v184 offset:20480
	ds_read_b128 v[208:211], v184 offset:21504
	ds_read_b128 v[212:215], v184 offset:22528
	ds_read_b128 v[216:219], v184 offset:23552
	s_cselect_b32 s51, s43, s57
	global_load_lds_dwordx4 v172, s[86:87]
	s_mov_b32 m0, s63
	s_nop 0
	global_load_lds_dwordx4 v174, s[86:87]
	s_mov_b64 s[86:87], s[52:53]
	s_mov_b32 m0, s64
	s_cselect_b32 s50, s42, s56
	s_nop 0
	global_load_lds_dwordx4 v172, s[86:87]
	s_mov_b32 m0, s65
	s_nop 0
	global_load_lds_dwordx4 v174, s[86:87]
	s_mov_b64 s[86:87], s[50:51]
	s_mov_b32 m0, s61
	s_nop 0
	global_load_lds_dwordx4 v175, s[86:87]
	s_mov_b32 m0, s66
	s_nop 0
	global_load_lds_dwordx4 v176, s[86:87]
	s_waitcnt vmcnt(8)
	s_waitcnt lgkmcnt(0)
	s_cselect_b32 s87, s41, s83
	s_cselect_b32 s86, s40, s82
	s_barrier
	s_setprio 0
	v_mfma_f32_16x16x128_f8f6f4 v[92:95], v[16:23], v[188:195], v[92:95]
	v_mfma_f32_16x16x128_f8f6f4 v[84:87], v[24:31], v[188:195], v[84:87]
	v_mfma_f32_16x16x128_f8f6f4 v[76:79], v[16:23], v[196:203], v[76:79]
	v_mfma_f32_16x16x128_f8f6f4 v[68:71], v[24:31], v[196:203], v[68:71]
	v_mfma_f32_16x16x128_f8f6f4 v[220:223], v[16:23], v[204:211], v[44:47]
	v_mfma_f32_16x16x128_f8f6f4 v[224:227], v[24:31], v[204:211], v[52:55]
	v_mfma_f32_16x16x128_f8f6f4 v[228:231], v[16:23], v[212:219], v[60:63]
	v_mfma_f32_16x16x128_f8f6f4 v[232:235], v[24:31], v[212:219], v[36:39]
	s_setprio 1
	s_setprio 0
	v_mfma_f32_16x16x128_f8f6f4 v[88:91], v[0:7], v[188:195], v[88:91]
	v_mfma_f32_16x16x128_f8f6f4 v[80:83], v[8:15], v[188:195], v[80:83]
	v_mfma_f32_16x16x128_f8f6f4 v[72:75], v[0:7], v[196:203], v[72:75]
	v_mfma_f32_16x16x128_f8f6f4 v[64:67], v[8:15], v[196:203], v[64:67]
	v_mfma_f32_16x16x128_f8f6f4 v[236:239], v[0:7], v[204:211], v[40:43]
	v_mfma_f32_16x16x128_f8f6f4 v[240:243], v[8:15], v[204:211], v[48:51]
	v_mfma_f32_16x16x128_f8f6f4 v[244:247], v[0:7], v[212:219], v[56:59]
	v_mfma_f32_16x16x128_f8f6f4 v[248:251], v[8:15], v[212:219], v[32:35]
	s_setprio 1
	s_add_i32 s85, 0, 0x18000
	s_add_i32 s88, 0, 0x1c000
	s_barrier
	v_add_u32_e32 v12, s85, v180
	v_add_u32_e32 v28, s88, v180
	ds_read_b128 v[0:3], v12
	ds_read_b128 v[4:7], v12 offset:1024
	ds_read_b128 v[8:11], v12 offset:2048
	ds_read_b128 v[12:15], v12 offset:3072
	ds_read_b128 v[16:19], v28
	ds_read_b128 v[20:23], v28 offset:1024
	ds_read_b128 v[24:27], v28 offset:2048
	ds_read_b128 v[28:31], v28 offset:3072
	v_mov_b32_e32 v165, v177
	v_mov_b32_e32 v187, v178
	s_mov_b32 m0, s67
	ds_read_b128 v[32:35], v184 offset:32768
	ds_read_b128 v[36:39], v184 offset:33792
	ds_read_b128 v[40:43], v184 offset:34816
	ds_read_b128 v[44:47], v184 offset:35840
	ds_read_b128 v[48:51], v184 offset:36864
	ds_read_b128 v[52:55], v184 offset:37888
	ds_read_b128 v[56:59], v184 offset:38912
	ds_read_b128 v[60:63], v184 offset:39936
	s_nop 0
	global_load_lds_dwordx4 v165, s[86:87]
	s_mov_b32 m0, s68
	s_nop 0
	global_load_lds_dwordx4 v187, s[86:87]
	s_waitcnt vmcnt(8)
	s_waitcnt lgkmcnt(0)
	s_barrier
	s_setprio 0
	v_mfma_f32_16x16x128_f8f6f4 v[156:159], v[0:7], v[32:39], v[156:159]
	v_mfma_f32_16x16x128_f8f6f4 v[148:151], v[8:15], v[32:39], v[148:151]
	v_mfma_f32_16x16x128_f8f6f4 v[140:143], v[0:7], v[40:47], v[140:143]
	v_mfma_f32_16x16x128_f8f6f4 v[132:135], v[8:15], v[40:47], v[132:135]
	v_mfma_f32_16x16x128_f8f6f4 v[124:127], v[0:7], v[48:55], v[124:127]
	v_mfma_f32_16x16x128_f8f6f4 v[116:119], v[8:15], v[48:55], v[116:119]
	v_mfma_f32_16x16x128_f8f6f4 v[108:111], v[0:7], v[56:63], v[108:111]
	v_mfma_f32_16x16x128_f8f6f4 v[100:103], v[8:15], v[56:63], v[100:103]
	s_setprio 1
	s_setprio 0
	v_mfma_f32_16x16x128_f8f6f4 v[152:155], v[16:23], v[32:39], v[152:155]
	v_mfma_f32_16x16x128_f8f6f4 v[144:147], v[24:31], v[32:39], v[144:147]
	v_mfma_f32_16x16x128_f8f6f4 v[136:139], v[16:23], v[40:47], v[136:139]
	v_mfma_f32_16x16x128_f8f6f4 v[128:131], v[24:31], v[40:47], v[128:131]
	v_mfma_f32_16x16x128_f8f6f4 v[120:123], v[16:23], v[48:55], v[120:123]
	v_mfma_f32_16x16x128_f8f6f4 v[112:115], v[24:31], v[48:55], v[112:115]
	v_mfma_f32_16x16x128_f8f6f4 v[104:107], v[16:23], v[56:63], v[104:107]
	v_mfma_f32_16x16x128_f8f6f4 v[96:99], v[24:31], v[56:63], v[96:99]
	s_setprio 1
	s_add_u32 s54, s54, 0x80
	s_addc_u32 s55, s55, 0
	s_add_i32 s85, s85, s60
	s_barrier
	s_mov_b32 m0, s85
	ds_read_b128 v[188:191], v184 offset:49152
	ds_read_b128 v[192:195], v184 offset:50176
	ds_read_b128 v[196:199], v184 offset:51200
	ds_read_b128 v[200:203], v184 offset:52224
	ds_read_b128 v[204:207], v184 offset:53248
	ds_read_b128 v[208:211], v184 offset:54272
	ds_read_b128 v[212:215], v184 offset:55296
	ds_read_b128 v[216:219], v184 offset:56320
	s_nop 0
	global_load_lds_dwordx4 v172, s[54:55]
	s_add_i32 m0, s85, 0x2000
	s_add_u32 s52, s52, 0x80
	global_load_lds_dwordx4 v174, s[54:55]
	s_addc_u32 s53, s53, 0
	s_add_i32 s54, s88, s60
	s_mov_b32 m0, s54
	s_nop 0
	global_load_lds_dwordx4 v172, s[52:53]
	s_add_i32 m0, s54, 0x2000
	s_add_u32 s50, s50, 0x80
	global_load_lds_dwordx4 v174, s[52:53]
	s_addc_u32 s51, s51, 0
	s_mov_b32 m0, s73
	s_nop 0
	global_load_lds_dwordx4 v175, s[50:51]
	s_mov_b32 m0, s74
	s_nop 0
	global_load_lds_dwordx4 v176, s[50:51]
	s_waitcnt vmcnt(8)
	s_waitcnt lgkmcnt(0)
	s_barrier
	s_setprio 0
	v_mfma_f32_16x16x128_f8f6f4 v[92:95], v[0:7], v[188:195], v[92:95]
	v_mfma_f32_16x16x128_f8f6f4 v[84:87], v[8:15], v[188:195], v[84:87]
	v_mfma_f32_16x16x128_f8f6f4 v[76:79], v[0:7], v[196:203], v[76:79]
	v_mfma_f32_16x16x128_f8f6f4 v[68:71], v[8:15], v[196:203], v[68:71]
	v_mfma_f32_16x16x128_f8f6f4 v[44:47], v[0:7], v[204:211], v[220:223]
	v_mfma_f32_16x16x128_f8f6f4 v[52:55], v[8:15], v[204:211], v[224:227]
	v_mfma_f32_16x16x128_f8f6f4 v[60:63], v[0:7], v[212:219], v[228:231]
	v_mfma_f32_16x16x128_f8f6f4 v[36:39], v[8:15], v[212:219], v[232:235]
	s_setprio 1
	s_setprio 0
	v_mfma_f32_16x16x128_f8f6f4 v[88:91], v[16:23], v[188:195], v[88:91]
	v_mfma_f32_16x16x128_f8f6f4 v[80:83], v[24:31], v[188:195], v[80:83]
	v_mfma_f32_16x16x128_f8f6f4 v[72:75], v[16:23], v[196:203], v[72:75]
	v_mfma_f32_16x16x128_f8f6f4 v[64:67], v[24:31], v[196:203], v[64:67]
	v_mfma_f32_16x16x128_f8f6f4 v[40:43], v[16:23], v[204:211], v[236:239]
	v_mfma_f32_16x16x128_f8f6f4 v[48:51], v[24:31], v[204:211], v[240:243]
	v_mfma_f32_16x16x128_f8f6f4 v[56:59], v[16:23], v[212:219], v[244:247]
	v_mfma_f32_16x16x128_f8f6f4 v[32:35], v[24:31], v[212:219], v[248:251]
	s_setprio 1
	s_add_u32 s47, s47, 0x100
	s_addc_u32 s79, s79, 0
	s_add_u32 s80, s80, 0x100
	s_addc_u32 s81, s81, 0
	s_add_u32 s56, s56, 0x100
	s_addc_u32 s57, s57, 0
	s_add_u32 s82, s82, 0x100
	s_addc_u32 s83, s83, 0
	s_cmp_ge_i32 s84, s0
	s_barrier
	s_cbranch_scc1 .LBB0_2282
.LBB0_2279:
	ds_read_b128 v[16:19], v182
	ds_read_b128 v[20:23], v182 offset:1024
	ds_read_b128 v[24:27], v182 offset:2048
	ds_read_b128 v[28:31], v182 offset:3072
	ds_read_b128 v[0:3], v183
	ds_read_b128 v[4:7], v183 offset:1024
	ds_read_b128 v[8:11], v183 offset:2048
	ds_read_b128 v[12:15], v183 offset:3072
	s_cmp_eq_u32 s75, s84
	s_cselect_b64 s[50:51], -1, 0
	s_add_u32 s52, s82, 0xffffff80
	s_addc_u32 s53, s83, -1
	v_mov_b32_e32 v165, v177
	v_mov_b32_e32 v187, v178
	s_add_i32 m0, s61, 0xc000
	ds_read_b128 v[188:191], v184
	ds_read_b128 v[192:195], v184 offset:1024
	ds_read_b128 v[196:199], v184 offset:2048
	ds_read_b128 v[200:203], v184 offset:3072
	ds_read_b128 v[204:207], v184 offset:4096
	ds_read_b128 v[208:211], v184 offset:5120
	ds_read_b128 v[212:215], v184 offset:6144
	ds_read_b128 v[216:219], v184 offset:7168
	s_nop 0
	global_load_lds_dwordx4 v165, s[52:53]
	s_add_i32 m0, s61, 0xe000
	s_nop 0
	global_load_lds_dwordx4 v187, s[52:53]
	s_waitcnt vmcnt(8)
	s_waitcnt lgkmcnt(0)
	s_barrier
	s_setprio 0
	v_mfma_f32_16x16x128_f8f6f4 v[156:159], v[16:23], v[188:195], v[156:159]
	v_mfma_f32_16x16x128_f8f6f4 v[148:151], v[24:31], v[188:195], v[148:151]
	v_mfma_f32_16x16x128_f8f6f4 v[140:143], v[16:23], v[196:203], v[140:143]
	v_mfma_f32_16x16x128_f8f6f4 v[132:135], v[24:31], v[196:203], v[132:135]
	v_mfma_f32_16x16x128_f8f6f4 v[124:127], v[16:23], v[204:211], v[124:127]
	v_mfma_f32_16x16x128_f8f6f4 v[116:119], v[24:31], v[204:211], v[116:119]
	v_mfma_f32_16x16x128_f8f6f4 v[108:111], v[16:23], v[212:219], v[108:111]
	v_mfma_f32_16x16x128_f8f6f4 v[100:103], v[24:31], v[212:219], v[100:103]
	s_setprio 1
	s_setprio 0
	v_mfma_f32_16x16x128_f8f6f4 v[152:155], v[0:7], v[188:195], v[152:155]
	v_mfma_f32_16x16x128_f8f6f4 v[144:147], v[8:15], v[188:195], v[144:147]
	v_mfma_f32_16x16x128_f8f6f4 v[136:139], v[0:7], v[196:203], v[136:139]
	v_mfma_f32_16x16x128_f8f6f4 v[128:131], v[8:15], v[196:203], v[128:131]
	v_mfma_f32_16x16x128_f8f6f4 v[120:123], v[0:7], v[204:211], v[120:123]
	v_mfma_f32_16x16x128_f8f6f4 v[112:115], v[8:15], v[204:211], v[112:115]
	v_mfma_f32_16x16x128_f8f6f4 v[104:107], v[0:7], v[212:219], v[104:107]
	v_mfma_f32_16x16x128_f8f6f4 v[96:99], v[8:15], v[212:219], v[96:99]
	s_setprio 1
	s_and_b64 s[52:53], s[48:49], s[50:51]
	s_andn2_b64 vcc, exec, s[52:53]
	s_barrier
	s_cbranch_vccnz .LBB0_2278
	v_lshl_add_u32 v175, v252, 11, v171
	v_lshl_add_u32 v176, v253, 11, v173
	v_lshl_add_u32 v178, v168, 11, v173
	v_lshl_add_u32 v177, v166, 11, v171
	s_branch .LBB0_2278

.LBB0_2365:
	ds_read_b128 v[154:157], v186
	ds_read_b128 v[158:161], v186 offset:1024
	ds_read_b128 v[16:19], v186 offset:2048
	ds_read_b128 v[20:23], v186 offset:3072
	ds_read_b128 v[162:165], v187
	ds_read_b128 v[166:169], v187 offset:1024
	ds_read_b128 v[0:3], v187 offset:2048
	ds_read_b128 v[4:7], v187 offset:3072
	s_add_i32 s84, s48, 2
	s_add_u32 s52, s82, 0xffffff80
	s_addc_u32 s53, s83, -1
	s_add_i32 m0, s58, 0xc000
	s_add_i32 s85, s58, 0xe000
	s_cmp_eq_u32 s71, s48
	s_cselect_b32 s48, s40, s80
	s_cselect_b32 s49, s41, s81
	s_cselect_b32 s51, s39, s47
	s_cselect_b32 s50, s38, s45
	s_cselect_b32 s55, s35, s83
	s_cselect_b32 s54, s34, s82
	ds_read_b128 v[170:173], v188
	ds_read_b128 v[174:177], v188 offset:1024
	ds_read_b128 v[190:193], v188 offset:2048
	ds_read_b128 v[194:197], v188 offset:3072
	ds_read_b128 v[198:201], v188 offset:4096
	ds_read_b128 v[202:205], v188 offset:5120
	ds_read_b128 v[8:11], v188 offset:6144
	ds_read_b128 v[12:15], v188 offset:7168
	s_nop 0
	global_load_lds_dwordx4 v180, s[52:53]
	s_mov_b32 m0, s85
	s_nop 0
	global_load_lds_dwordx4 v182, s[52:53]
	s_waitcnt vmcnt(8)
	s_waitcnt lgkmcnt(0)
	s_barrier
	s_setprio 0
	v_mfma_f32_16x16x128_f8f6f4 v[132:135], v[154:161], v[8:15], v[132:135]
	v_mfma_f32_16x16x128_f8f6f4 v[230:233], v[154:161], v[190:197], v[144:147]
	v_mfma_f32_16x16x128_f8f6f4 v[234:237], v[154:161], v[198:205], v[140:143]
	s_setprio 1
	s_setprio 0
	v_mfma_f32_16x16x128_f8f6f4 v[108:111], v[162:169], v[190:197], v[108:111]
	v_mfma_f32_16x16x128_f8f6f4 v[96:99], v[162:169], v[198:205], v[96:99]
	v_mfma_f32_16x16x128_f8f6f4 v[76:79], v[162:169], v[8:15], v[76:79]
	s_setprio 1
	s_cselect_b32 s53, s37, s79
	s_cselect_b32 s52, s36, s78
	s_add_i32 s85, s72, s57
	s_barrier
	s_mov_b64 s[86:87], s[50:51]
	s_mov_b32 m0, s85
	ds_read_b128 v[140:143], v188 offset:16384
	ds_read_b128 v[144:147], v188 offset:17408
	ds_read_b128 v[206:209], v188 offset:18432
	ds_read_b128 v[210:213], v188 offset:19456
	ds_read_b128 v[214:217], v188 offset:20480
	ds_read_b128 v[218:221], v188 offset:21504
	ds_read_b128 v[222:225], v188 offset:22528
	ds_read_b128 v[226:229], v188 offset:23552
	global_load_lds_dwordx4 v179, s[86:87]
	s_add_i32 m0, s85, 0x2000
	s_add_i32 s85, s73, s57
	global_load_lds_dwordx4 v181, s[86:87]
	s_mov_b64 s[86:87], s[52:53]
	v_mov_b32_e32 v153, v181
	s_mov_b32 m0, s85
	v_mfma_f32_16x16x128_f8f6f4 v[238:241], v[0:7], v[170:177], v[88:91]
	global_load_lds_dwordx4 v179, s[86:87]
	s_add_i32 m0, s85, 0x2000
	s_nop 0
	global_load_lds_dwordx4 v153, s[86:87]
	s_nop 2
	s_mov_b64 s[86:87], s[48:49]
	s_mov_b32 m0, s58
	v_mfma_f32_16x16x128_f8f6f4 v[148:151], v[154:161], v[170:177], v[148:151]
	global_load_lds_dwordx4 v180, s[86:87]
	s_mov_b32 m0, s59
	s_nop 0
	global_load_lds_dwordx4 v182, s[86:87]
	s_waitcnt vmcnt(8)
	v_mfma_f32_16x16x128_f8f6f4 v[136:139], v[16:23], v[190:197], v[136:139]
	s_waitcnt lgkmcnt(0)
	s_barrier
	v_mfma_f32_16x16x128_f8f6f4 v[124:127], v[16:23], v[8:15], v[124:127]
	v_mfma_f32_16x16x128_f8f6f4 v[242:245], v[0:7], v[198:205], v[100:103]
	s_setprio 0
	s_waitcnt lgkmcnt(0)
	v_mfma_f32_16x16x128_f8f6f4 v[128:131], v[154:161], v[140:147], v[128:131]
	v_mfma_f32_16x16x128_f8f6f4 v[120:123], v[154:161], v[206:213], v[120:123]
	v_mfma_f32_16x16x128_f8f6f4 v[116:119], v[154:161], v[214:221], v[116:119]
	v_mfma_f32_16x16x128_f8f6f4 v[112:115], v[154:161], v[222:229], v[112:115]
	s_setprio 1
	s_setprio 0
	v_mfma_f32_16x16x128_f8f6f4 v[68:71], v[162:169], v[140:147], v[68:71]
	v_mfma_f32_16x16x128_f8f6f4 v[64:67], v[162:169], v[206:213], v[64:67]
	v_mfma_f32_16x16x128_f8f6f4 v[52:55], v[162:169], v[214:221], v[52:55]
	v_mfma_f32_16x16x128_f8f6f4 v[48:51], v[162:169], v[222:229], v[48:51]
	s_setprio 1
	s_add_i32 s85, 0, 0x18000
	s_add_i32 s86, 0, 0x1c000
	s_barrier
	v_mfma_f32_16x16x128_f8f6f4 v[80:83], v[16:23], v[198:205], v[80:83]
	v_add_u32_e32 v88, s85, v184
	ds_read_b128 v[154:157], v88
	ds_read_b128 v[158:161], v88 offset:1024
	v_mfma_f32_16x16x128_f8f6f4 v[40:43], v[0:7], v[190:197], v[40:43]
	v_mfma_f32_16x16x128_f8f6f4 v[92:95], v[16:23], v[214:221], v[92:95]
	v_mfma_f32_16x16x128_f8f6f4 v[56:59], v[0:7], v[140:147], v[56:59]
	v_mfma_f32_16x16x128_f8f6f4 v[36:39], v[0:7], v[214:221], v[36:39]
	v_mfma_f32_16x16x128_f8f6f4 v[44:47], v[162:169], v[170:177], v[44:47]
	ds_read_b128 v[162:165], v88 offset:2048
	ds_read_b128 v[166:169], v88 offset:3072
	v_mfma_f32_16x16x128_f8f6f4 v[250:253], v[16:23], v[206:213], v[84:87]
	s_nop 6
	v_add_u32_e32 v84, s86, v184
	v_mfma_f32_16x16x128_f8f6f4 v[32:35], v[0:7], v[206:213], v[32:35]
	ds_read_b128 v[190:193], v84
	ds_read_b128 v[194:197], v84 offset:1024
	ds_read_b128 v[198:201], v84 offset:2048
	ds_read_b128 v[202:205], v84 offset:3072
	v_mfma_f32_16x16x128_f8f6f4 v[246:249], v[16:23], v[140:147], v[104:107]
	s_mov_b32 m0, s60
	ds_read_b128 v[84:87], v188 offset:32768
	ds_read_b128 v[88:91], v188 offset:33792
	ds_read_b128 v[100:103], v188 offset:34816
	s_nop 0
	ds_read_b128 v[104:107], v188 offset:35840
	ds_read_b128 v[206:209], v188 offset:36864
	ds_read_b128 v[210:213], v188 offset:37888
	ds_read_b128 v[214:217], v188 offset:38912
	ds_read_b128 v[218:221], v188 offset:39936
	v_mfma_f32_16x16x128_f8f6f4 v[72:75], v[16:23], v[170:177], v[72:75]
	global_load_lds_dwordx4 v180, s[54:55]
	s_mov_b32 m0, s61
	s_nop 0
	global_load_lds_dwordx4 v182, s[54:55]
	s_waitcnt vmcnt(8)
	v_mfma_f32_16x16x128_f8f6f4 v[60:63], v[16:23], v[222:229], v[60:63]
	s_waitcnt lgkmcnt(0)
	s_barrier
	s_setprio 0
	v_mfma_f32_16x16x128_f8f6f4 v[144:147], v[154:161], v[100:107], v[230:233]
	v_mfma_f32_16x16x128_f8f6f4 v[140:143], v[154:161], v[206:213], v[234:237]
	v_mfma_f32_16x16x128_f8f6f4 v[132:135], v[154:161], v[214:221], v[132:135]
	s_setprio 1
	s_setprio 0
	v_mfma_f32_16x16x128_f8f6f4 v[108:111], v[190:197], v[100:107], v[108:111]
	v_mfma_f32_16x16x128_f8f6f4 v[96:99], v[190:197], v[206:213], v[96:99]
	v_mfma_f32_16x16x128_f8f6f4 v[76:79], v[190:197], v[214:221], v[76:79]
	s_setprio 1
	s_add_u32 s50, s50, 0x80
	s_addc_u32 s51, s51, 0
	s_add_i32 s54, s85, s57
	s_barrier
	v_mfma_f32_16x16x128_f8f6f4 v[148:151], v[154:161], v[84:91], v[148:151]
	s_mov_b32 m0, s54
	v_mfma_f32_16x16x128_f8f6f4 v[72:75], v[162:169], v[84:91], v[72:75]
	v_mfma_f32_16x16x128_f8f6f4 v[44:47], v[190:197], v[84:91], v[44:47]
	v_mfma_f32_16x16x128_f8f6f4 v[88:91], v[198:205], v[84:91], v[238:241]
	v_mfma_f32_16x16x128_f8f6f4 v[28:31], v[0:7], v[8:15], v[28:31]
	v_mfma_f32_16x16x128_f8f6f4 v[24:27], v[0:7], v[222:229], v[24:27]
	ds_read_b128 v[0:3], v188 offset:49152
	ds_read_b128 v[4:7], v188 offset:50176
	ds_read_b128 v[8:11], v188 offset:51200
	ds_read_b128 v[12:15], v188 offset:52224
	ds_read_b128 v[16:19], v188 offset:53248
	ds_read_b128 v[20:23], v188 offset:54272
	ds_read_b128 v[170:173], v188 offset:55296
	ds_read_b128 v[174:177], v188 offset:56320
	s_nop 0
	global_load_lds_dwordx4 v179, s[50:51]
	s_add_i32 m0, s54, 0x2000
	s_nop 0
	global_load_lds_dwordx4 v181, s[50:51]
	s_add_u32 s50, s52, 0x80
	s_addc_u32 s51, s53, 0
	s_add_i32 s52, s86, s57
	s_mov_b32 m0, s52
	v_mfma_f32_16x16x128_f8f6f4 v[136:139], v[162:169], v[100:107], v[136:139]
	global_load_lds_dwordx4 v179, s[50:51]
	s_add_i32 m0, s52, 0x2000
	s_add_u32 s48, s48, 0x80
	global_load_lds_dwordx4 v181, s[50:51]
	s_addc_u32 s49, s49, 0
	v_mfma_f32_16x16x128_f8f6f4 v[40:43], v[198:205], v[100:107], v[40:43]
	s_mov_b32 m0, s69
	s_nop 0
	global_load_lds_dwordx4 v180, s[48:49]
	s_mov_b32 m0, s70
	v_mfma_f32_16x16x128_f8f6f4 v[80:83], v[162:169], v[206:213], v[80:83]
	global_load_lds_dwordx4 v182, s[48:49]
	s_waitcnt vmcnt(8)
	s_waitcnt lgkmcnt(0)
	s_barrier
	v_mfma_f32_16x16x128_f8f6f4 v[124:127], v[162:169], v[214:221], v[124:127]
	v_mfma_f32_16x16x128_f8f6f4 v[100:103], v[198:205], v[206:213], v[242:245]
	v_mfma_f32_16x16x128_f8f6f4 v[28:31], v[198:205], v[214:221], v[28:31]
	s_setprio 0
	s_waitcnt lgkmcnt(0)
	v_mfma_f32_16x16x128_f8f6f4 v[128:131], v[154:161], v[0:7], v[128:131]
	v_mfma_f32_16x16x128_f8f6f4 v[104:107], v[162:169], v[0:7], v[246:249]
	v_mfma_f32_16x16x128_f8f6f4 v[120:123], v[154:161], v[8:15], v[120:123]
	v_mfma_f32_16x16x128_f8f6f4 v[84:87], v[162:169], v[8:15], v[250:253]
	v_mfma_f32_16x16x128_f8f6f4 v[116:119], v[154:161], v[16:23], v[116:119]
	v_mfma_f32_16x16x128_f8f6f4 v[92:95], v[162:169], v[16:23], v[92:95]
	v_mfma_f32_16x16x128_f8f6f4 v[112:115], v[154:161], v[170:177], v[112:115]
	v_mfma_f32_16x16x128_f8f6f4 v[60:63], v[162:169], v[170:177], v[60:63]
	s_setprio 1
	s_setprio 0
	v_mfma_f32_16x16x128_f8f6f4 v[68:71], v[190:197], v[0:7], v[68:71]
	v_mfma_f32_16x16x128_f8f6f4 v[56:59], v[198:205], v[0:7], v[56:59]
	v_mfma_f32_16x16x128_f8f6f4 v[64:67], v[190:197], v[8:15], v[64:67]
	v_mfma_f32_16x16x128_f8f6f4 v[32:35], v[198:205], v[8:15], v[32:35]
	v_mfma_f32_16x16x128_f8f6f4 v[52:55], v[190:197], v[16:23], v[52:55]
	v_mfma_f32_16x16x128_f8f6f4 v[36:39], v[198:205], v[16:23], v[36:39]
	v_mfma_f32_16x16x128_f8f6f4 v[48:51], v[190:197], v[170:177], v[48:51]
	v_mfma_f32_16x16x128_f8f6f4 v[24:27], v[198:205], v[170:177], v[24:27]
	s_setprio 1
	s_add_u32 s45, s45, 0x100
	s_addc_u32 s47, s47, 0
	s_add_u32 s78, s78, 0x100
	s_addc_u32 s79, s79, 0
	s_add_u32 s80, s80, 0x100
	s_addc_u32 s81, s81, 0
	s_add_u32 s82, s82, 0x100
	s_addc_u32 s83, s83, 0
	s_cmp_ge_i32 s84, s0
	s_mov_b32 s48, s84
	s_barrier
	s_cbranch_scc0 .LBB0_2365
	v_pk_mul_f32 v[162:163], v[150:151], s[18:19] op_sel_hi:[1,0]
	v_pk_mul_f32 v[164:165], v[148:149], s[18:19] op_sel_hi:[1,0]
	v_pk_mul_f32 v[166:167], v[74:75], s[18:19] op_sel_hi:[1,0]
	v_pk_mul_f32 v[168:169], v[72:73], s[18:19] op_sel_hi:[1,0]
	v_pk_mul_f32 v[170:171], v[146:147], s[18:19] op_sel_hi:[1,0]
	v_pk_mul_f32 v[172:173], v[144:145], s[18:19] op_sel_hi:[1,0]
	v_pk_mul_f32 v[174:175], v[138:139], s[18:19] op_sel_hi:[1,0]
	v_pk_mul_f32 v[176:177], v[136:137], s[18:19] op_sel_hi:[1,0]
	v_pk_mul_f32 v[160:161], v[142:143], s[18:19] op_sel_hi:[1,0]
	v_pk_mul_f32 v[158:159], v[140:141], s[18:19] op_sel_hi:[1,0]
	v_pk_mul_f32 v[146:147], v[82:83], s[18:19] op_sel_hi:[1,0]
	v_pk_mul_f32 v[156:157], v[80:81], s[18:19] op_sel_hi:[1,0]
	v_pk_mul_f32 v[144:145], v[134:135], s[18:19] op_sel_hi:[1,0]
	v_pk_mul_f32 v[142:143], v[132:133], s[18:19] op_sel_hi:[1,0]
	v_pk_mul_f32 v[132:133], v[126:127], s[18:19] op_sel_hi:[1,0]
	v_pk_mul_f32 v[140:141], v[124:125], s[18:19] op_sel_hi:[1,0]
	v_pk_mul_f32 v[154:155], v[130:131], s[18:19] op_sel_hi:[1,0]
	v_pk_mul_f32 v[150:151], v[128:129], s[18:19] op_sel_hi:[1,0]
	v_pk_mul_f32 v[138:139], v[106:107], s[18:19] op_sel_hi:[1,0]
	v_pk_mul_f32 v[148:149], v[104:105], s[18:19] op_sel_hi:[1,0]
	v_pk_mul_f32 v[136:137], v[122:123], s[18:19] op_sel_hi:[1,0]
	v_pk_mul_f32 v[134:135], v[120:121], s[18:19] op_sel_hi:[1,0]
	v_pk_mul_f32 v[128:129], v[86:87], s[18:19] op_sel_hi:[1,0]
	v_pk_mul_f32 v[130:131], v[84:85], s[18:19] op_sel_hi:[1,0]
	v_pk_mul_f32 v[126:127], v[118:119], s[18:19] op_sel_hi:[1,0]
	v_pk_mul_f32 v[124:125], v[116:117], s[18:19] op_sel_hi:[1,0]
	v_pk_mul_f32 v[120:121], v[94:95], s[18:19] op_sel_hi:[1,0]
	v_pk_mul_f32 v[122:123], v[92:93], s[18:19] op_sel_hi:[1,0]
	v_pk_mul_f32 v[118:119], v[114:115], s[18:19] op_sel_hi:[1,0]
	v_pk_mul_f32 v[116:117], v[112:113], s[18:19] op_sel_hi:[1,0]
	v_pk_mul_f32 v[112:113], v[62:63], s[18:19] op_sel_hi:[1,0]
	v_pk_mul_f32 v[114:115], v[60:61], s[18:19] op_sel_hi:[1,0]
	v_pk_mul_f32 v[84:85], v[46:47], s[18:19] op_sel_hi:[1,0]
	v_pk_mul_f32 v[86:87], v[44:45], s[18:19] op_sel_hi:[1,0]
	v_pk_mul_f32 v[90:91], v[90:91], s[18:19] op_sel_hi:[1,0]
	v_pk_mul_f32 v[88:89], v[88:89], s[18:19] op_sel_hi:[1,0]
	v_pk_mul_f32 v[92:93], v[110:111], s[18:19] op_sel_hi:[1,0]
	v_pk_mul_f32 v[94:95], v[108:109], s[18:19] op_sel_hi:[1,0]
	v_pk_mul_f32 v[104:105], v[42:43], s[18:19] op_sel_hi:[1,0]
	v_pk_mul_f32 v[106:107], v[40:41], s[18:19] op_sel_hi:[1,0]
	v_pk_mul_f32 v[82:83], v[98:99], s[18:19] op_sel_hi:[1,0]
	v_pk_mul_f32 v[80:81], v[96:97], s[18:19] op_sel_hi:[1,0]
	v_pk_mul_f32 v[46:47], v[102:103], s[18:19] op_sel_hi:[1,0]
	v_pk_mul_f32 v[74:75], v[100:101], s[18:19] op_sel_hi:[1,0]
	v_pk_mul_f32 v[72:73], v[78:79], s[18:19] op_sel_hi:[1,0]
	v_pk_mul_f32 v[62:63], v[76:77], s[18:19] op_sel_hi:[1,0]
	v_pk_mul_f32 v[30:31], v[30:31], s[18:19] op_sel_hi:[1,0]
	v_pk_mul_f32 v[60:61], v[28:29], s[18:19] op_sel_hi:[1,0]
	v_pk_mul_f32 v[70:71], v[70:71], s[18:19] op_sel_hi:[1,0]
	v_pk_mul_f32 v[68:69], v[68:69], s[18:19] op_sel_hi:[1,0]
	v_pk_mul_f32 v[40:41], v[58:59], s[18:19] op_sel_hi:[1,0]
	v_pk_mul_f32 v[56:57], v[56:57], s[18:19] op_sel_hi:[1,0]
	v_pk_mul_f32 v[44:45], v[66:67], s[18:19] op_sel_hi:[1,0]
	v_pk_mul_f32 v[42:43], v[64:65], s[18:19] op_sel_hi:[1,0]
	v_pk_mul_f32 v[28:29], v[34:35], s[18:19] op_sel_hi:[1,0]
	v_pk_mul_f32 v[32:33], v[32:33], s[18:19] op_sel_hi:[1,0]
	v_pk_mul_f32 v[22:23], v[54:55], s[18:19] op_sel_hi:[1,0]
	v_pk_mul_f32 v[20:21], v[52:53], s[18:19] op_sel_hi:[1,0]
	v_pk_mul_f32 v[10:11], v[38:39], s[18:19] op_sel_hi:[1,0]
	v_pk_mul_f32 v[18:19], v[36:37], s[18:19] op_sel_hi:[1,0]
	v_pk_mul_f32 v[16:17], v[50:51], s[18:19] op_sel_hi:[1,0]
	v_pk_mul_f32 v[14:15], v[48:49], s[18:19] op_sel_hi:[1,0]
	v_pk_mul_f32 v[8:9], v[26:27], s[18:19] op_sel_hi:[1,0]
	v_pk_mul_f32 v[12:13], v[24:25], s[18:19] op_sel_hi:[1,0]
	s_and_b64 vcc, exec, s[16:17]
	s_cbranch_vccz .LBB0_2368
